# final phase written by hand: all 28 loads of a two-row pass issued together and one pass ahead of the arithmetic (the compiler fetched x1 one 1 KiB piece at a time), g_post_ffn loaded once
# speedup vs baseline: 1.0043x; 1.0043x over previous
; DI int tidx() { int t = threadIdx.x & 255; asm volatile("" : "+v"(t)); return t; }
; DI float bflo(unsigned u) { return __uint_as_float(u << 16); }
; DI float bfhi(unsigned u) { return __uint_as_float(u & 0xffff0000u); }
; DI void phase_final(const Params& p, int bid, int nb) {
;   const int lane = tidx() & 63, gw = bid * 4 + (tidx() >> 6), nw = nb * 4;
;   const float* mod = (const float*)(p.ws + WS_MOD);
;   const bf16_t* y2 = (const bf16_t*)(p.ws + WS_Y2); const float* ssq = (const float*)(p.ws + WS_SSQ);
;   for (int row0 = gw * 2; row0 < T_; row0 += nw * 2) {
;     const int b = row0 >> 13;
;     f32x4 ov[2][4], yv[2][4]; float ss[2] = {0.f, 0.f};
; #pragma unroll
;     for (int r = 0; r < 2; ++r) {
; #pragma unroll
;       for (int i = 0; i < 4; ++i) { ov[r][i] = ((const f32x4*)(p.out + (size_t)(row0 + r) * 1024))[lane + 64 * i];
;         const u32x2 yb = *(const u32x2*)(y2 + (size_t)(row0 + r) * 1024 + 4 * lane + 256 * i); yv[r][i] = (f32x4){bflo(yb[0]), bfhi(yb[0]), bflo(yb[1]), bfhi(yb[1])}; }
; #pragma unroll
;       for (int x = 0; x < 8; ++x) ss[r] += ssq[(size_t)x * T_ + row0 + r];
.LBB0_1941:
	s_or_b64 exec, exec, s[0:1]
	v_mov_b32_e32 v1, v206
	s_waitcnt lgkmcnt(0)
	s_barrier
	s_mov_b32 s0, 0x8000
	v_ashrrev_i32_e32 v0, 5, v206
	v_and_b32_e32 v0, -2, v0
	v_add_u32_e32 v0, v0, v208
	v_cmp_gt_i32_e32 vcc, s0, v0
	s_and_saveexec_b64 s[0:1], vcc
	s_cbranch_execz .LBB0_1944
	v_and_b32_e32 v10, 63, v206
	v_readfirstlane_b32 s2, v0
	v_lshlrev_b32_e32 v2, 4, v10
	v_lshlrev_b32_e32 v3, 3, v10
	v_mov_b32_e32 v28, 0x0
	v_mov_b32_e32 v29, 0x20000
	v_mov_b32_e32 v30, 0x40000
	v_mov_b32_e32 v31, 0x60000
	v_mov_b32_e32 v32, 0x80000
	v_mov_b32_e32 v33, 0xa0000
	v_mov_b32_e32 v34, 0xc0000
	v_mov_b32_e32 v35, 0xe0000
	global_load_dwordx4 v[12:15], v2, s[54:55] offset:0
	global_load_dwordx4 v[16:19], v2, s[54:55] offset:1024
	global_load_dwordx4 v[20:23], v2, s[54:55] offset:2048
	global_load_dwordx4 v[24:27], v2, s[54:55] offset:3072
	s_mov_b32 s14, 0x3a800000
	s_mov_b32 s15, 0x3a800000
	s_mov_b32 s22, 0x800000
	v_mov_b32_e32 v230, 0x358637bd
	v_mov_b32_e32 v231, 0x358637bd
	s_add_u32 s12, s2, 0x0
	s_lshl_b32 s13, s12, 12
	s_add_u32 s4, s66, s13
	s_addc_u32 s5, s67, 0
	s_add_u32 s4, s4, 0x1000
	s_addc_u32 s5, s5, 0
	s_lshl_b32 s13, s12, 11
	s_add_u32 s6, s84, s13
	s_addc_u32 s7, s85, 0
	s_add_u32 s6, s6, 0x6000000
	s_addc_u32 s7, s7, 0
	s_lshl_b32 s13, s12, 2
	s_add_u32 s8, s84, s13
	s_addc_u32 s9, s85, 0
	s_add_u32 s8, s8, 0x3000000
	s_addc_u32 s9, s9, 0
	s_lshr_b32 s13, s12, 13
	s_mul_i32 s13, s13, 0x6000
	s_add_u32 s10, s84, s13
	s_addc_u32 s11, s85, 0
	s_add_u32 s10, s10, 0x105000
	s_addc_u32 s11, s11, 0
	global_load_dwordx2 v[88:89], v28, s[8:9]
	global_load_dwordx2 v[90:91], v29, s[8:9]
	global_load_dwordx2 v[92:93], v30, s[8:9]
	global_load_dwordx2 v[94:95], v31, s[8:9]
	global_load_dwordx2 v[96:97], v32, s[8:9]
	global_load_dwordx2 v[98:99], v33, s[8:9]
	global_load_dwordx2 v[100:101], v34, s[8:9]
	global_load_dwordx2 v[102:103], v35, s[8:9]
	global_load_dwordx2 v[72:73], v3, s[6:7] offset:0
	global_load_dwordx2 v[74:75], v3, s[6:7] offset:512
	global_load_dwordx2 v[76:77], v3, s[6:7] offset:1024
	global_load_dwordx2 v[78:79], v3, s[6:7] offset:1536
	global_load_dwordx2 v[80:81], v3, s[6:7] offset:2048
	global_load_dwordx2 v[82:83], v3, s[6:7] offset:2560
	global_load_dwordx2 v[84:85], v3, s[6:7] offset:3072
	global_load_dwordx2 v[86:87], v3, s[6:7] offset:3584
	global_load_dwordx4 v[104:107], v2, s[10:11] offset:0
	global_load_dwordx4 v[108:111], v2, s[10:11] offset:1024
	global_load_dwordx4 v[112:115], v2, s[10:11] offset:2048
	global_load_dwordx4 v[116:119], v2, s[10:11] offset:3072
	global_load_dwordx4 v[40:43], v2, s[4:5] offset:-4096
	global_load_dwordx4 v[44:47], v2, s[4:5] offset:-3072
	global_load_dwordx4 v[48:51], v2, s[4:5] offset:-2048
	global_load_dwordx4 v[52:55], v2, s[4:5] offset:-1024
	global_load_dwordx4 v[56:59], v2, s[4:5] offset:0
	global_load_dwordx4 v[60:63], v2, s[4:5] offset:1024
	global_load_dwordx4 v[64:67], v2, s[4:5] offset:2048
	global_load_dwordx4 v[68:71], v2, s[4:5] offset:3072
	s_add_u32 s12, s2, 0x1000
	s_lshl_b32 s13, s12, 12
	s_add_u32 s16, s66, s13
	s_addc_u32 s17, s67, 0
	s_add_u32 s16, s16, 0x1000
	s_addc_u32 s17, s17, 0
	s_lshl_b32 s13, s12, 11
	s_add_u32 s6, s84, s13
	s_addc_u32 s7, s85, 0
	s_add_u32 s6, s6, 0x6000000
	s_addc_u32 s7, s7, 0
	s_lshl_b32 s13, s12, 2
	s_add_u32 s8, s84, s13
	s_addc_u32 s9, s85, 0
	s_add_u32 s8, s8, 0x3000000
	s_addc_u32 s9, s9, 0
	s_lshr_b32 s13, s12, 13
	s_mul_i32 s13, s13, 0x6000
	s_add_u32 s10, s84, s13
	s_addc_u32 s11, s85, 0
	s_add_u32 s10, s10, 0x105000
	s_addc_u32 s11, s11, 0
	global_load_dwordx2 v[172:173], v28, s[8:9]
	global_load_dwordx2 v[174:175], v29, s[8:9]
	global_load_dwordx2 v[176:177], v30, s[8:9]
	global_load_dwordx2 v[178:179], v31, s[8:9]
	global_load_dwordx2 v[180:181], v32, s[8:9]
	global_load_dwordx2 v[182:183], v33, s[8:9]
	global_load_dwordx2 v[184:185], v34, s[8:9]
	global_load_dwordx2 v[186:187], v35, s[8:9]
	global_load_dwordx2 v[156:157], v3, s[6:7] offset:0
	global_load_dwordx2 v[158:159], v3, s[6:7] offset:512
	global_load_dwordx2 v[160:161], v3, s[6:7] offset:1024
	global_load_dwordx2 v[162:163], v3, s[6:7] offset:1536
	global_load_dwordx2 v[164:165], v3, s[6:7] offset:2048
	global_load_dwordx2 v[166:167], v3, s[6:7] offset:2560
	global_load_dwordx2 v[168:169], v3, s[6:7] offset:3072
	global_load_dwordx2 v[170:171], v3, s[6:7] offset:3584
	global_load_dwordx4 v[188:191], v2, s[10:11] offset:0
	global_load_dwordx4 v[192:195], v2, s[10:11] offset:1024
	global_load_dwordx4 v[196:199], v2, s[10:11] offset:2048
	global_load_dwordx4 v[200:203], v2, s[10:11] offset:3072
	global_load_dwordx4 v[124:127], v2, s[16:17] offset:-4096
	global_load_dwordx4 v[128:131], v2, s[16:17] offset:-3072
	global_load_dwordx4 v[132:135], v2, s[16:17] offset:-2048
	global_load_dwordx4 v[136:139], v2, s[16:17] offset:-1024
	global_load_dwordx4 v[140:143], v2, s[16:17] offset:0
	global_load_dwordx4 v[144:147], v2, s[16:17] offset:1024
	global_load_dwordx4 v[148:151], v2, s[16:17] offset:2048
	global_load_dwordx4 v[152:155], v2, s[16:17] offset:3072
	s_waitcnt vmcnt(28)
; DI void phase_final(const Params& p, int bid, int nb) {
;     ...
;       for (int x = 0; x < 8; ++x) ss[r] += ssq[(size_t)x * T_ + row0 + r];
;     }
; #pragma unroll
;     for (int r = 0; r < 2; ++r) {
;       const float rstd = rsqrtf(ss[r] * (1.f / 1024.f) + 1e-6f);
;       f32x4* orow = (f32x4*)(p.out + (size_t)(row0 + r) * 1024);
; #pragma unroll
;       for (int i = 0; i < 4; ++i) {
;         const int col = 4 * lane + 256 * i;
;         const f32x4 g4 = *(const f32x4*)(p.g_post_ffn + col), gt = *(const f32x4*)(mod + b * 6144 + 5120 + col);
;         orow[lane + 64 * i] = ov[r][i] + gt * (yv[r][i] * rstd * g4);
	v_pk_add_f32 v[88:89], v[88:89], 0 op_sel_hi:[1,0]
	v_pk_add_f32 v[88:89], v[88:89], v[90:91]
	v_pk_add_f32 v[88:89], v[88:89], v[92:93]
	v_pk_add_f32 v[88:89], v[88:89], v[94:95]
	v_pk_add_f32 v[88:89], v[88:89], v[96:97]
	v_pk_add_f32 v[88:89], v[88:89], v[98:99]
	v_pk_add_f32 v[88:89], v[88:89], v[100:101]
	v_pk_add_f32 v[88:89], v[88:89], v[102:103]
	v_pk_fma_f32 v[88:89], v[88:89], s[14:15], v[230:231]
	v_mul_f32_e32 v210, 0x4b800000, v88
	v_cmp_gt_f32_e32 vcc, s22, v88
	s_nop 1
	v_cndmask_b32_e32 v210, v88, v210, vcc
	v_rsq_f32_e32 v210, v210
	s_nop 0
	v_mul_f32_e32 v211, 0x45800000, v210
	v_cndmask_b32_e32 v226, v210, v211, vcc
	v_mul_f32_e32 v210, 0x4b800000, v89
	v_cmp_gt_f32_e32 vcc, s22, v89
	s_nop 1
	v_cndmask_b32_e32 v210, v89, v210, vcc
	v_rsq_f32_e32 v210, v210
	s_nop 0
	v_mul_f32_e32 v211, 0x45800000, v210
	v_cndmask_b32_e32 v228, v210, v211, vcc
	v_lshlrev_b32_e32 v212, 16, v72
	v_and_b32_e32 v213, 0xffff0000, v72
	v_lshlrev_b32_e32 v214, 16, v73
	v_and_b32_e32 v215, 0xffff0000, v73
	v_pk_mul_f32 v[212:213], v[226:227], v[212:213] op_sel_hi:[0,1]
	v_pk_mul_f32 v[214:215], v[226:227], v[214:215] op_sel_hi:[0,1]
	v_pk_mul_f32 v[212:213], v[212:213], v[12:13]
	v_pk_mul_f32 v[214:215], v[214:215], v[14:15]
	v_pk_fma_f32 v[40:41], v[104:105], v[212:213], v[40:41]
	v_pk_fma_f32 v[42:43], v[106:107], v[214:215], v[42:43]
	global_store_dwordx4 v2, v[40:43], s[4:5] offset:-4096
	v_lshlrev_b32_e32 v216, 16, v74
	v_and_b32_e32 v217, 0xffff0000, v74
	v_lshlrev_b32_e32 v218, 16, v75
	v_and_b32_e32 v219, 0xffff0000, v75
	v_pk_mul_f32 v[216:217], v[226:227], v[216:217] op_sel_hi:[0,1]
	v_pk_mul_f32 v[218:219], v[226:227], v[218:219] op_sel_hi:[0,1]
	v_pk_mul_f32 v[216:217], v[216:217], v[16:17]
	v_pk_mul_f32 v[218:219], v[218:219], v[18:19]
	v_pk_fma_f32 v[44:45], v[108:109], v[216:217], v[44:45]
	v_pk_fma_f32 v[46:47], v[110:111], v[218:219], v[46:47]
	global_store_dwordx4 v2, v[44:47], s[4:5] offset:-3072
	v_lshlrev_b32_e32 v212, 16, v76
	v_and_b32_e32 v213, 0xffff0000, v76
	v_lshlrev_b32_e32 v214, 16, v77
	v_and_b32_e32 v215, 0xffff0000, v77
	v_pk_mul_f32 v[212:213], v[226:227], v[212:213] op_sel_hi:[0,1]
	v_pk_mul_f32 v[214:215], v[226:227], v[214:215] op_sel_hi:[0,1]
	v_pk_mul_f32 v[212:213], v[212:213], v[20:21]
	v_pk_mul_f32 v[214:215], v[214:215], v[22:23]
	v_pk_fma_f32 v[48:49], v[112:113], v[212:213], v[48:49]
	v_pk_fma_f32 v[50:51], v[114:115], v[214:215], v[50:51]
	global_store_dwordx4 v2, v[48:51], s[4:5] offset:-2048
	v_lshlrev_b32_e32 v216, 16, v78
	v_and_b32_e32 v217, 0xffff0000, v78
	v_lshlrev_b32_e32 v218, 16, v79
	v_and_b32_e32 v219, 0xffff0000, v79
	v_pk_mul_f32 v[216:217], v[226:227], v[216:217] op_sel_hi:[0,1]
	v_pk_mul_f32 v[218:219], v[226:227], v[218:219] op_sel_hi:[0,1]
	v_pk_mul_f32 v[216:217], v[216:217], v[24:25]
	v_pk_mul_f32 v[218:219], v[218:219], v[26:27]
	v_pk_fma_f32 v[52:53], v[116:117], v[216:217], v[52:53]
	v_pk_fma_f32 v[54:55], v[118:119], v[218:219], v[54:55]
	global_store_dwordx4 v2, v[52:55], s[4:5] offset:-1024
	v_lshlrev_b32_e32 v212, 16, v80
	v_and_b32_e32 v213, 0xffff0000, v80
	v_lshlrev_b32_e32 v214, 16, v81
	v_and_b32_e32 v215, 0xffff0000, v81
	v_pk_mul_f32 v[212:213], v[228:229], v[212:213] op_sel_hi:[0,1]
	v_pk_mul_f32 v[214:215], v[228:229], v[214:215] op_sel_hi:[0,1]
	v_pk_mul_f32 v[212:213], v[212:213], v[12:13]
	v_pk_mul_f32 v[214:215], v[214:215], v[14:15]
	v_pk_fma_f32 v[56:57], v[104:105], v[212:213], v[56:57]
	v_pk_fma_f32 v[58:59], v[106:107], v[214:215], v[58:59]
	global_store_dwordx4 v2, v[56:59], s[4:5] offset:0
	v_lshlrev_b32_e32 v216, 16, v82
	v_and_b32_e32 v217, 0xffff0000, v82
	v_lshlrev_b32_e32 v218, 16, v83
	v_and_b32_e32 v219, 0xffff0000, v83
	v_pk_mul_f32 v[216:217], v[228:229], v[216:217] op_sel_hi:[0,1]
	v_pk_mul_f32 v[218:219], v[228:229], v[218:219] op_sel_hi:[0,1]
	v_pk_mul_f32 v[216:217], v[216:217], v[16:17]
	v_pk_mul_f32 v[218:219], v[218:219], v[18:19]
	v_pk_fma_f32 v[60:61], v[108:109], v[216:217], v[60:61]
	v_pk_fma_f32 v[62:63], v[110:111], v[218:219], v[62:63]
	global_store_dwordx4 v2, v[60:63], s[4:5] offset:1024
	v_lshlrev_b32_e32 v212, 16, v84
	v_and_b32_e32 v213, 0xffff0000, v84
	v_lshlrev_b32_e32 v214, 16, v85
	v_and_b32_e32 v215, 0xffff0000, v85
	v_pk_mul_f32 v[212:213], v[228:229], v[212:213] op_sel_hi:[0,1]
	v_pk_mul_f32 v[214:215], v[228:229], v[214:215] op_sel_hi:[0,1]
	v_pk_mul_f32 v[212:213], v[212:213], v[20:21]
	v_pk_mul_f32 v[214:215], v[214:215], v[22:23]
	v_pk_fma_f32 v[64:65], v[112:113], v[212:213], v[64:65]
	v_pk_fma_f32 v[66:67], v[114:115], v[214:215], v[66:67]
	global_store_dwordx4 v2, v[64:67], s[4:5] offset:2048
	v_lshlrev_b32_e32 v216, 16, v86
	v_and_b32_e32 v217, 0xffff0000, v86
	v_lshlrev_b32_e32 v218, 16, v87
	v_and_b32_e32 v219, 0xffff0000, v87
	v_pk_mul_f32 v[216:217], v[228:229], v[216:217] op_sel_hi:[0,1]
	v_pk_mul_f32 v[218:219], v[228:229], v[218:219] op_sel_hi:[0,1]
	v_pk_mul_f32 v[216:217], v[216:217], v[24:25]
	v_pk_mul_f32 v[218:219], v[218:219], v[26:27]
	v_pk_fma_f32 v[68:69], v[116:117], v[216:217], v[68:69]
	v_pk_fma_f32 v[70:71], v[118:119], v[218:219], v[70:71]
	global_store_dwordx4 v2, v[68:71], s[4:5] offset:3072
	s_add_u32 s12, s2, 0x2000
	s_lshl_b32 s13, s12, 12
	s_add_u32 s4, s66, s13
	s_addc_u32 s5, s67, 0
	s_add_u32 s4, s4, 0x1000
	s_addc_u32 s5, s5, 0
	s_lshl_b32 s13, s12, 11
	s_add_u32 s6, s84, s13
	s_addc_u32 s7, s85, 0
	s_add_u32 s6, s6, 0x6000000
	s_addc_u32 s7, s7, 0
	s_lshl_b32 s13, s12, 2
	s_add_u32 s8, s84, s13
	s_addc_u32 s9, s85, 0
	s_add_u32 s8, s8, 0x3000000
	s_addc_u32 s9, s9, 0
	s_lshr_b32 s13, s12, 13
	s_mul_i32 s13, s13, 0x6000
	s_add_u32 s10, s84, s13
	s_addc_u32 s11, s85, 0
; DI float bflo(unsigned u) { return __uint_as_float(u << 16); }
; DI float bfhi(unsigned u) { return __uint_as_float(u & 0xffff0000u); }
; DI void phase_final(const Params& p, int bid, int nb) {
;     ...
;     f32x4 ov[2][4], yv[2][4]; float ss[2] = {0.f, 0.f};
; #pragma unroll
;     for (int r = 0; r < 2; ++r) {
; #pragma unroll
;       for (int i = 0; i < 4; ++i) { ov[r][i] = ((const f32x4*)(p.out + (size_t)(row0 + r) * 1024))[lane + 64 * i];
;         const u32x2 yb = *(const u32x2*)(y2 + (size_t)(row0 + r) * 1024 + 4 * lane + 256 * i); yv[r][i] = (f32x4){bflo(yb[0]), bfhi(yb[0]), bflo(yb[1]), bfhi(yb[1])}; }
; #pragma unroll
;       for (int x = 0; x < 8; ++x) ss[r] += ssq[(size_t)x * T_ + row0 + r];
;     }
; #pragma unroll
;     for (int r = 0; r < 2; ++r) {
;       const float rstd = rsqrtf(ss[r] * (1.f / 1024.f) + 1e-6f);
;       f32x4* orow = (f32x4*)(p.out + (size_t)(row0 + r) * 1024);
; #pragma unroll
;       for (int i = 0; i < 4; ++i) {
;         const int col = 4 * lane + 256 * i;
;         const f32x4 g4 = *(const f32x4*)(p.g_post_ffn + col), gt = *(const f32x4*)(mod + b * 6144 + 5120 + col);
;         orow[lane + 64 * i] = ov[r][i] + gt * (yv[r][i] * rstd * g4);
	s_add_u32 s10, s10, 0x105000
	s_addc_u32 s11, s11, 0
	global_load_dwordx2 v[88:89], v28, s[8:9]
	global_load_dwordx2 v[90:91], v29, s[8:9]
	global_load_dwordx2 v[92:93], v30, s[8:9]
	global_load_dwordx2 v[94:95], v31, s[8:9]
	global_load_dwordx2 v[96:97], v32, s[8:9]
	global_load_dwordx2 v[98:99], v33, s[8:9]
	global_load_dwordx2 v[100:101], v34, s[8:9]
	global_load_dwordx2 v[102:103], v35, s[8:9]
	global_load_dwordx2 v[72:73], v3, s[6:7] offset:0
	global_load_dwordx2 v[74:75], v3, s[6:7] offset:512
	global_load_dwordx2 v[76:77], v3, s[6:7] offset:1024
	global_load_dwordx2 v[78:79], v3, s[6:7] offset:1536
	global_load_dwordx2 v[80:81], v3, s[6:7] offset:2048
	global_load_dwordx2 v[82:83], v3, s[6:7] offset:2560
	global_load_dwordx2 v[84:85], v3, s[6:7] offset:3072
	global_load_dwordx2 v[86:87], v3, s[6:7] offset:3584
	global_load_dwordx4 v[104:107], v2, s[10:11] offset:0
	global_load_dwordx4 v[108:111], v2, s[10:11] offset:1024
	global_load_dwordx4 v[112:115], v2, s[10:11] offset:2048
	global_load_dwordx4 v[116:119], v2, s[10:11] offset:3072
	global_load_dwordx4 v[40:43], v2, s[4:5] offset:-4096
	global_load_dwordx4 v[44:47], v2, s[4:5] offset:-3072
	global_load_dwordx4 v[48:51], v2, s[4:5] offset:-2048
	global_load_dwordx4 v[52:55], v2, s[4:5] offset:-1024
	global_load_dwordx4 v[56:59], v2, s[4:5] offset:0
	global_load_dwordx4 v[60:63], v2, s[4:5] offset:1024
	global_load_dwordx4 v[64:67], v2, s[4:5] offset:2048
	global_load_dwordx4 v[68:71], v2, s[4:5] offset:3072
	s_waitcnt vmcnt(28)
	v_pk_add_f32 v[172:173], v[172:173], 0 op_sel_hi:[1,0]
	v_pk_add_f32 v[172:173], v[172:173], v[174:175]
	v_pk_add_f32 v[172:173], v[172:173], v[176:177]
	v_pk_add_f32 v[172:173], v[172:173], v[178:179]
	v_pk_add_f32 v[172:173], v[172:173], v[180:181]
	v_pk_add_f32 v[172:173], v[172:173], v[182:183]
	v_pk_add_f32 v[172:173], v[172:173], v[184:185]
	v_pk_add_f32 v[172:173], v[172:173], v[186:187]
	v_pk_fma_f32 v[172:173], v[172:173], s[14:15], v[230:231]
	v_mul_f32_e32 v210, 0x4b800000, v172
	v_cmp_gt_f32_e32 vcc, s22, v172
	s_nop 1
	v_cndmask_b32_e32 v210, v172, v210, vcc
	v_rsq_f32_e32 v210, v210
	s_nop 0
	v_mul_f32_e32 v211, 0x45800000, v210
	v_cndmask_b32_e32 v226, v210, v211, vcc
	v_mul_f32_e32 v210, 0x4b800000, v173
	v_cmp_gt_f32_e32 vcc, s22, v173
	s_nop 1
	v_cndmask_b32_e32 v210, v173, v210, vcc
	v_rsq_f32_e32 v210, v210
	s_nop 0
	v_mul_f32_e32 v211, 0x45800000, v210
	v_cndmask_b32_e32 v228, v210, v211, vcc
	v_lshlrev_b32_e32 v212, 16, v156
	v_and_b32_e32 v213, 0xffff0000, v156
	v_lshlrev_b32_e32 v214, 16, v157
	v_and_b32_e32 v215, 0xffff0000, v157
	v_pk_mul_f32 v[212:213], v[226:227], v[212:213] op_sel_hi:[0,1]
	v_pk_mul_f32 v[214:215], v[226:227], v[214:215] op_sel_hi:[0,1]
	v_pk_mul_f32 v[212:213], v[212:213], v[12:13]
	v_pk_mul_f32 v[214:215], v[214:215], v[14:15]
	v_pk_fma_f32 v[124:125], v[188:189], v[212:213], v[124:125]
	v_pk_fma_f32 v[126:127], v[190:191], v[214:215], v[126:127]
	global_store_dwordx4 v2, v[124:127], s[16:17] offset:-4096
	v_lshlrev_b32_e32 v216, 16, v158
	v_and_b32_e32 v217, 0xffff0000, v158
	v_lshlrev_b32_e32 v218, 16, v159
	v_and_b32_e32 v219, 0xffff0000, v159
	v_pk_mul_f32 v[216:217], v[226:227], v[216:217] op_sel_hi:[0,1]
	v_pk_mul_f32 v[218:219], v[226:227], v[218:219] op_sel_hi:[0,1]
	v_pk_mul_f32 v[216:217], v[216:217], v[16:17]
	v_pk_mul_f32 v[218:219], v[218:219], v[18:19]
	v_pk_fma_f32 v[128:129], v[192:193], v[216:217], v[128:129]
	v_pk_fma_f32 v[130:131], v[194:195], v[218:219], v[130:131]
	global_store_dwordx4 v2, v[128:131], s[16:17] offset:-3072
	v_lshlrev_b32_e32 v212, 16, v160
	v_and_b32_e32 v213, 0xffff0000, v160
	v_lshlrev_b32_e32 v214, 16, v161
	v_and_b32_e32 v215, 0xffff0000, v161
	v_pk_mul_f32 v[212:213], v[226:227], v[212:213] op_sel_hi:[0,1]
	v_pk_mul_f32 v[214:215], v[226:227], v[214:215] op_sel_hi:[0,1]
	v_pk_mul_f32 v[212:213], v[212:213], v[20:21]
	v_pk_mul_f32 v[214:215], v[214:215], v[22:23]
	v_pk_fma_f32 v[132:133], v[196:197], v[212:213], v[132:133]
	v_pk_fma_f32 v[134:135], v[198:199], v[214:215], v[134:135]
	global_store_dwordx4 v2, v[132:135], s[16:17] offset:-2048
	v_lshlrev_b32_e32 v216, 16, v162
	v_and_b32_e32 v217, 0xffff0000, v162
	v_lshlrev_b32_e32 v218, 16, v163
	v_and_b32_e32 v219, 0xffff0000, v163
	v_pk_mul_f32 v[216:217], v[226:227], v[216:217] op_sel_hi:[0,1]
	v_pk_mul_f32 v[218:219], v[226:227], v[218:219] op_sel_hi:[0,1]
	v_pk_mul_f32 v[216:217], v[216:217], v[24:25]
	v_pk_mul_f32 v[218:219], v[218:219], v[26:27]
	v_pk_fma_f32 v[136:137], v[200:201], v[216:217], v[136:137]
	v_pk_fma_f32 v[138:139], v[202:203], v[218:219], v[138:139]
	global_store_dwordx4 v2, v[136:139], s[16:17] offset:-1024
	v_lshlrev_b32_e32 v212, 16, v164
	v_and_b32_e32 v213, 0xffff0000, v164
	v_lshlrev_b32_e32 v214, 16, v165
	v_and_b32_e32 v215, 0xffff0000, v165
	v_pk_mul_f32 v[212:213], v[228:229], v[212:213] op_sel_hi:[0,1]
	v_pk_mul_f32 v[214:215], v[228:229], v[214:215] op_sel_hi:[0,1]
	v_pk_mul_f32 v[212:213], v[212:213], v[12:13]
	v_pk_mul_f32 v[214:215], v[214:215], v[14:15]
	v_pk_fma_f32 v[140:141], v[188:189], v[212:213], v[140:141]
	v_pk_fma_f32 v[142:143], v[190:191], v[214:215], v[142:143]
	global_store_dwordx4 v2, v[140:143], s[16:17] offset:0
	v_lshlrev_b32_e32 v216, 16, v166
	v_and_b32_e32 v217, 0xffff0000, v166
	v_lshlrev_b32_e32 v218, 16, v167
	v_and_b32_e32 v219, 0xffff0000, v167
	v_pk_mul_f32 v[216:217], v[228:229], v[216:217] op_sel_hi:[0,1]
	v_pk_mul_f32 v[218:219], v[228:229], v[218:219] op_sel_hi:[0,1]
	v_pk_mul_f32 v[216:217], v[216:217], v[16:17]
	v_pk_mul_f32 v[218:219], v[218:219], v[18:19]
	v_pk_fma_f32 v[144:145], v[192:193], v[216:217], v[144:145]
; DI float bflo(unsigned u) { return __uint_as_float(u << 16); }
; DI float bfhi(unsigned u) { return __uint_as_float(u & 0xffff0000u); }
; DI void phase_final(const Params& p, int bid, int nb) {
;     ...
;     f32x4 ov[2][4], yv[2][4]; float ss[2] = {0.f, 0.f};
; #pragma unroll
;     for (int r = 0; r < 2; ++r) {
; #pragma unroll
;       for (int i = 0; i < 4; ++i) { ov[r][i] = ((const f32x4*)(p.out + (size_t)(row0 + r) * 1024))[lane + 64 * i];
;         const u32x2 yb = *(const u32x2*)(y2 + (size_t)(row0 + r) * 1024 + 4 * lane + 256 * i); yv[r][i] = (f32x4){bflo(yb[0]), bfhi(yb[0]), bflo(yb[1]), bfhi(yb[1])}; }
; #pragma unroll
;       for (int x = 0; x < 8; ++x) ss[r] += ssq[(size_t)x * T_ + row0 + r];
;     }
; #pragma unroll
;     for (int r = 0; r < 2; ++r) {
;       const float rstd = rsqrtf(ss[r] * (1.f / 1024.f) + 1e-6f);
;       f32x4* orow = (f32x4*)(p.out + (size_t)(row0 + r) * 1024);
; #pragma unroll
;       for (int i = 0; i < 4; ++i) {
;         const int col = 4 * lane + 256 * i;
;         const f32x4 g4 = *(const f32x4*)(p.g_post_ffn + col), gt = *(const f32x4*)(mod + b * 6144 + 5120 + col);
;         orow[lane + 64 * i] = ov[r][i] + gt * (yv[r][i] * rstd * g4);
	v_pk_fma_f32 v[146:147], v[194:195], v[218:219], v[146:147]
	global_store_dwordx4 v2, v[144:147], s[16:17] offset:1024
	v_lshlrev_b32_e32 v212, 16, v168
	v_and_b32_e32 v213, 0xffff0000, v168
	v_lshlrev_b32_e32 v214, 16, v169
	v_and_b32_e32 v215, 0xffff0000, v169
	v_pk_mul_f32 v[212:213], v[228:229], v[212:213] op_sel_hi:[0,1]
	v_pk_mul_f32 v[214:215], v[228:229], v[214:215] op_sel_hi:[0,1]
	v_pk_mul_f32 v[212:213], v[212:213], v[20:21]
	v_pk_mul_f32 v[214:215], v[214:215], v[22:23]
	v_pk_fma_f32 v[148:149], v[196:197], v[212:213], v[148:149]
	v_pk_fma_f32 v[150:151], v[198:199], v[214:215], v[150:151]
	global_store_dwordx4 v2, v[148:151], s[16:17] offset:2048
	v_lshlrev_b32_e32 v216, 16, v170
	v_and_b32_e32 v217, 0xffff0000, v170
	v_lshlrev_b32_e32 v218, 16, v171
	v_and_b32_e32 v219, 0xffff0000, v171
	v_pk_mul_f32 v[216:217], v[228:229], v[216:217] op_sel_hi:[0,1]
	v_pk_mul_f32 v[218:219], v[228:229], v[218:219] op_sel_hi:[0,1]
	v_pk_mul_f32 v[216:217], v[216:217], v[24:25]
	v_pk_mul_f32 v[218:219], v[218:219], v[26:27]
	v_pk_fma_f32 v[152:153], v[200:201], v[216:217], v[152:153]
	v_pk_fma_f32 v[154:155], v[202:203], v[218:219], v[154:155]
	global_store_dwordx4 v2, v[152:155], s[16:17] offset:3072
	s_add_u32 s12, s2, 0x3000
	s_lshl_b32 s13, s12, 12
	s_add_u32 s16, s66, s13
	s_addc_u32 s17, s67, 0
	s_add_u32 s16, s16, 0x1000
	s_addc_u32 s17, s17, 0
	s_lshl_b32 s13, s12, 11
	s_add_u32 s6, s84, s13
	s_addc_u32 s7, s85, 0
	s_add_u32 s6, s6, 0x6000000
	s_addc_u32 s7, s7, 0
	s_lshl_b32 s13, s12, 2
	s_add_u32 s8, s84, s13
	s_addc_u32 s9, s85, 0
	s_add_u32 s8, s8, 0x3000000
	s_addc_u32 s9, s9, 0
	s_lshr_b32 s13, s12, 13
	s_mul_i32 s13, s13, 0x6000
	s_add_u32 s10, s84, s13
	s_addc_u32 s11, s85, 0
	s_add_u32 s10, s10, 0x105000
	s_addc_u32 s11, s11, 0
	global_load_dwordx2 v[172:173], v28, s[8:9]
	global_load_dwordx2 v[174:175], v29, s[8:9]
	global_load_dwordx2 v[176:177], v30, s[8:9]
	global_load_dwordx2 v[178:179], v31, s[8:9]
	global_load_dwordx2 v[180:181], v32, s[8:9]
	global_load_dwordx2 v[182:183], v33, s[8:9]
	global_load_dwordx2 v[184:185], v34, s[8:9]
	global_load_dwordx2 v[186:187], v35, s[8:9]
	global_load_dwordx2 v[156:157], v3, s[6:7] offset:0
	global_load_dwordx2 v[158:159], v3, s[6:7] offset:512
	global_load_dwordx2 v[160:161], v3, s[6:7] offset:1024
	global_load_dwordx2 v[162:163], v3, s[6:7] offset:1536
	global_load_dwordx2 v[164:165], v3, s[6:7] offset:2048
	global_load_dwordx2 v[166:167], v3, s[6:7] offset:2560
	global_load_dwordx2 v[168:169], v3, s[6:7] offset:3072
	global_load_dwordx2 v[170:171], v3, s[6:7] offset:3584
	global_load_dwordx4 v[188:191], v2, s[10:11] offset:0
	global_load_dwordx4 v[192:195], v2, s[10:11] offset:1024
	global_load_dwordx4 v[196:199], v2, s[10:11] offset:2048
	global_load_dwordx4 v[200:203], v2, s[10:11] offset:3072
	global_load_dwordx4 v[124:127], v2, s[16:17] offset:-4096
	global_load_dwordx4 v[128:131], v2, s[16:17] offset:-3072
	global_load_dwordx4 v[132:135], v2, s[16:17] offset:-2048
	global_load_dwordx4 v[136:139], v2, s[16:17] offset:-1024
	global_load_dwordx4 v[140:143], v2, s[16:17] offset:0
	global_load_dwordx4 v[144:147], v2, s[16:17] offset:1024
	global_load_dwordx4 v[148:151], v2, s[16:17] offset:2048
	global_load_dwordx4 v[152:155], v2, s[16:17] offset:3072
	s_waitcnt vmcnt(28)
	v_pk_add_f32 v[88:89], v[88:89], 0 op_sel_hi:[1,0]
	v_pk_add_f32 v[88:89], v[88:89], v[90:91]
	v_pk_add_f32 v[88:89], v[88:89], v[92:93]
	v_pk_add_f32 v[88:89], v[88:89], v[94:95]
	v_pk_add_f32 v[88:89], v[88:89], v[96:97]
	v_pk_add_f32 v[88:89], v[88:89], v[98:99]
	v_pk_add_f32 v[88:89], v[88:89], v[100:101]
	v_pk_add_f32 v[88:89], v[88:89], v[102:103]
	v_pk_fma_f32 v[88:89], v[88:89], s[14:15], v[230:231]
	v_mul_f32_e32 v210, 0x4b800000, v88
	v_cmp_gt_f32_e32 vcc, s22, v88
	s_nop 1
	v_cndmask_b32_e32 v210, v88, v210, vcc
	v_rsq_f32_e32 v210, v210
	s_nop 0
	v_mul_f32_e32 v211, 0x45800000, v210
	v_cndmask_b32_e32 v226, v210, v211, vcc
	v_mul_f32_e32 v210, 0x4b800000, v89
	v_cmp_gt_f32_e32 vcc, s22, v89
	s_nop 1
	v_cndmask_b32_e32 v210, v89, v210, vcc
	v_rsq_f32_e32 v210, v210
	s_nop 0
	v_mul_f32_e32 v211, 0x45800000, v210
	v_cndmask_b32_e32 v228, v210, v211, vcc
	v_lshlrev_b32_e32 v212, 16, v72
	v_and_b32_e32 v213, 0xffff0000, v72
	v_lshlrev_b32_e32 v214, 16, v73
	v_and_b32_e32 v215, 0xffff0000, v73
	v_pk_mul_f32 v[212:213], v[226:227], v[212:213] op_sel_hi:[0,1]
	v_pk_mul_f32 v[214:215], v[226:227], v[214:215] op_sel_hi:[0,1]
	v_pk_mul_f32 v[212:213], v[212:213], v[12:13]
	v_pk_mul_f32 v[214:215], v[214:215], v[14:15]
	v_pk_fma_f32 v[40:41], v[104:105], v[212:213], v[40:41]
	v_pk_fma_f32 v[42:43], v[106:107], v[214:215], v[42:43]
	global_store_dwordx4 v2, v[40:43], s[4:5] offset:-4096
	v_lshlrev_b32_e32 v216, 16, v74
	v_and_b32_e32 v217, 0xffff0000, v74
	v_lshlrev_b32_e32 v218, 16, v75
	v_and_b32_e32 v219, 0xffff0000, v75
	v_pk_mul_f32 v[216:217], v[226:227], v[216:217] op_sel_hi:[0,1]
	v_pk_mul_f32 v[218:219], v[226:227], v[218:219] op_sel_hi:[0,1]
	v_pk_mul_f32 v[216:217], v[216:217], v[16:17]
	v_pk_mul_f32 v[218:219], v[218:219], v[18:19]
	v_pk_fma_f32 v[44:45], v[108:109], v[216:217], v[44:45]
	v_pk_fma_f32 v[46:47], v[110:111], v[218:219], v[46:47]
	global_store_dwordx4 v2, v[44:47], s[4:5] offset:-3072
	v_lshlrev_b32_e32 v212, 16, v76
	v_and_b32_e32 v213, 0xffff0000, v76
	v_lshlrev_b32_e32 v214, 16, v77
	v_and_b32_e32 v215, 0xffff0000, v77
	v_pk_mul_f32 v[212:213], v[226:227], v[212:213] op_sel_hi:[0,1]
	v_pk_mul_f32 v[214:215], v[226:227], v[214:215] op_sel_hi:[0,1]
	v_pk_mul_f32 v[212:213], v[212:213], v[20:21]
	v_pk_mul_f32 v[214:215], v[214:215], v[22:23]
	v_pk_fma_f32 v[48:49], v[112:113], v[212:213], v[48:49]
; DI float bflo(unsigned u) { return __uint_as_float(u << 16); }
; DI float bfhi(unsigned u) { return __uint_as_float(u & 0xffff0000u); }
; DI void phase_final(const Params& p, int bid, int nb) {
;     ...
;     f32x4 ov[2][4], yv[2][4]; float ss[2] = {0.f, 0.f};
; #pragma unroll
;     for (int r = 0; r < 2; ++r) {
; #pragma unroll
;       for (int i = 0; i < 4; ++i) { ov[r][i] = ((const f32x4*)(p.out + (size_t)(row0 + r) * 1024))[lane + 64 * i];
;         const u32x2 yb = *(const u32x2*)(y2 + (size_t)(row0 + r) * 1024 + 4 * lane + 256 * i); yv[r][i] = (f32x4){bflo(yb[0]), bfhi(yb[0]), bflo(yb[1]), bfhi(yb[1])}; }
; #pragma unroll
;       for (int x = 0; x < 8; ++x) ss[r] += ssq[(size_t)x * T_ + row0 + r];
;     }
; #pragma unroll
;     for (int r = 0; r < 2; ++r) {
;       const float rstd = rsqrtf(ss[r] * (1.f / 1024.f) + 1e-6f);
;       f32x4* orow = (f32x4*)(p.out + (size_t)(row0 + r) * 1024);
; #pragma unroll
;       for (int i = 0; i < 4; ++i) {
;         const int col = 4 * lane + 256 * i;
;         const f32x4 g4 = *(const f32x4*)(p.g_post_ffn + col), gt = *(const f32x4*)(mod + b * 6144 + 5120 + col);
;         orow[lane + 64 * i] = ov[r][i] + gt * (yv[r][i] * rstd * g4);
	v_pk_fma_f32 v[50:51], v[114:115], v[214:215], v[50:51]
	global_store_dwordx4 v2, v[48:51], s[4:5] offset:-2048
	v_lshlrev_b32_e32 v216, 16, v78
	v_and_b32_e32 v217, 0xffff0000, v78
	v_lshlrev_b32_e32 v218, 16, v79
	v_and_b32_e32 v219, 0xffff0000, v79
	v_pk_mul_f32 v[216:217], v[226:227], v[216:217] op_sel_hi:[0,1]
	v_pk_mul_f32 v[218:219], v[226:227], v[218:219] op_sel_hi:[0,1]
	v_pk_mul_f32 v[216:217], v[216:217], v[24:25]
	v_pk_mul_f32 v[218:219], v[218:219], v[26:27]
	v_pk_fma_f32 v[52:53], v[116:117], v[216:217], v[52:53]
	v_pk_fma_f32 v[54:55], v[118:119], v[218:219], v[54:55]
	global_store_dwordx4 v2, v[52:55], s[4:5] offset:-1024
	v_lshlrev_b32_e32 v212, 16, v80
	v_and_b32_e32 v213, 0xffff0000, v80
	v_lshlrev_b32_e32 v214, 16, v81
	v_and_b32_e32 v215, 0xffff0000, v81
	v_pk_mul_f32 v[212:213], v[228:229], v[212:213] op_sel_hi:[0,1]
	v_pk_mul_f32 v[214:215], v[228:229], v[214:215] op_sel_hi:[0,1]
	v_pk_mul_f32 v[212:213], v[212:213], v[12:13]
	v_pk_mul_f32 v[214:215], v[214:215], v[14:15]
	v_pk_fma_f32 v[56:57], v[104:105], v[212:213], v[56:57]
	v_pk_fma_f32 v[58:59], v[106:107], v[214:215], v[58:59]
	global_store_dwordx4 v2, v[56:59], s[4:5] offset:0
	v_lshlrev_b32_e32 v216, 16, v82
	v_and_b32_e32 v217, 0xffff0000, v82
	v_lshlrev_b32_e32 v218, 16, v83
	v_and_b32_e32 v219, 0xffff0000, v83
	v_pk_mul_f32 v[216:217], v[228:229], v[216:217] op_sel_hi:[0,1]
	v_pk_mul_f32 v[218:219], v[228:229], v[218:219] op_sel_hi:[0,1]
	v_pk_mul_f32 v[216:217], v[216:217], v[16:17]
	v_pk_mul_f32 v[218:219], v[218:219], v[18:19]
	v_pk_fma_f32 v[60:61], v[108:109], v[216:217], v[60:61]
	v_pk_fma_f32 v[62:63], v[110:111], v[218:219], v[62:63]
	global_store_dwordx4 v2, v[60:63], s[4:5] offset:1024
	v_lshlrev_b32_e32 v212, 16, v84
	v_and_b32_e32 v213, 0xffff0000, v84
	v_lshlrev_b32_e32 v214, 16, v85
	v_and_b32_e32 v215, 0xffff0000, v85
	v_pk_mul_f32 v[212:213], v[228:229], v[212:213] op_sel_hi:[0,1]
	v_pk_mul_f32 v[214:215], v[228:229], v[214:215] op_sel_hi:[0,1]
	v_pk_mul_f32 v[212:213], v[212:213], v[20:21]
	v_pk_mul_f32 v[214:215], v[214:215], v[22:23]
	v_pk_fma_f32 v[64:65], v[112:113], v[212:213], v[64:65]
	v_pk_fma_f32 v[66:67], v[114:115], v[214:215], v[66:67]
	global_store_dwordx4 v2, v[64:67], s[4:5] offset:2048
	v_lshlrev_b32_e32 v216, 16, v86
	v_and_b32_e32 v217, 0xffff0000, v86
	v_lshlrev_b32_e32 v218, 16, v87
	v_and_b32_e32 v219, 0xffff0000, v87
	v_pk_mul_f32 v[216:217], v[228:229], v[216:217] op_sel_hi:[0,1]
	v_pk_mul_f32 v[218:219], v[228:229], v[218:219] op_sel_hi:[0,1]
	v_pk_mul_f32 v[216:217], v[216:217], v[24:25]
	v_pk_mul_f32 v[218:219], v[218:219], v[26:27]
	v_pk_fma_f32 v[68:69], v[116:117], v[216:217], v[68:69]
	v_pk_fma_f32 v[70:71], v[118:119], v[218:219], v[70:71]
	global_store_dwordx4 v2, v[68:71], s[4:5] offset:3072
	s_add_u32 s12, s2, 0x4000
	s_lshl_b32 s13, s12, 12
	s_add_u32 s4, s66, s13
	s_addc_u32 s5, s67, 0
	s_add_u32 s4, s4, 0x1000
	s_addc_u32 s5, s5, 0
	s_lshl_b32 s13, s12, 11
	s_add_u32 s6, s84, s13
	s_addc_u32 s7, s85, 0
	s_add_u32 s6, s6, 0x6000000
	s_addc_u32 s7, s7, 0
	s_lshl_b32 s13, s12, 2
	s_add_u32 s8, s84, s13
	s_addc_u32 s9, s85, 0
	s_add_u32 s8, s8, 0x3000000
	s_addc_u32 s9, s9, 0
	s_lshr_b32 s13, s12, 13
	s_mul_i32 s13, s13, 0x6000
	s_add_u32 s10, s84, s13
	s_addc_u32 s11, s85, 0
	s_add_u32 s10, s10, 0x105000
	s_addc_u32 s11, s11, 0
	global_load_dwordx2 v[88:89], v28, s[8:9]
	global_load_dwordx2 v[90:91], v29, s[8:9]
	global_load_dwordx2 v[92:93], v30, s[8:9]
	global_load_dwordx2 v[94:95], v31, s[8:9]
	global_load_dwordx2 v[96:97], v32, s[8:9]
	global_load_dwordx2 v[98:99], v33, s[8:9]
	global_load_dwordx2 v[100:101], v34, s[8:9]
	global_load_dwordx2 v[102:103], v35, s[8:9]
	global_load_dwordx2 v[72:73], v3, s[6:7] offset:0
	global_load_dwordx2 v[74:75], v3, s[6:7] offset:512
	global_load_dwordx2 v[76:77], v3, s[6:7] offset:1024
	global_load_dwordx2 v[78:79], v3, s[6:7] offset:1536
	global_load_dwordx2 v[80:81], v3, s[6:7] offset:2048
	global_load_dwordx2 v[82:83], v3, s[6:7] offset:2560
	global_load_dwordx2 v[84:85], v3, s[6:7] offset:3072
	global_load_dwordx2 v[86:87], v3, s[6:7] offset:3584
	global_load_dwordx4 v[104:107], v2, s[10:11] offset:0
	global_load_dwordx4 v[108:111], v2, s[10:11] offset:1024
	global_load_dwordx4 v[112:115], v2, s[10:11] offset:2048
	global_load_dwordx4 v[116:119], v2, s[10:11] offset:3072
	global_load_dwordx4 v[40:43], v2, s[4:5] offset:-4096
	global_load_dwordx4 v[44:47], v2, s[4:5] offset:-3072
	global_load_dwordx4 v[48:51], v2, s[4:5] offset:-2048
	global_load_dwordx4 v[52:55], v2, s[4:5] offset:-1024
	global_load_dwordx4 v[56:59], v2, s[4:5] offset:0
	global_load_dwordx4 v[60:63], v2, s[4:5] offset:1024
	global_load_dwordx4 v[64:67], v2, s[4:5] offset:2048
	global_load_dwordx4 v[68:71], v2, s[4:5] offset:3072
	s_waitcnt vmcnt(28)
; DI float bflo(unsigned u) { return __uint_as_float(u << 16); }
; DI float bfhi(unsigned u) { return __uint_as_float(u & 0xffff0000u); }
; DI void phase_final(const Params& p, int bid, int nb) {
;     ...
;     f32x4 ov[2][4], yv[2][4]; float ss[2] = {0.f, 0.f};
; #pragma unroll
;     for (int r = 0; r < 2; ++r) {
; #pragma unroll
;       for (int i = 0; i < 4; ++i) { ov[r][i] = ((const f32x4*)(p.out + (size_t)(row0 + r) * 1024))[lane + 64 * i];
;         const u32x2 yb = *(const u32x2*)(y2 + (size_t)(row0 + r) * 1024 + 4 * lane + 256 * i); yv[r][i] = (f32x4){bflo(yb[0]), bfhi(yb[0]), bflo(yb[1]), bfhi(yb[1])}; }
; #pragma unroll
;       for (int x = 0; x < 8; ++x) ss[r] += ssq[(size_t)x * T_ + row0 + r];
;     }
; #pragma unroll
;     for (int r = 0; r < 2; ++r) {
;       const float rstd = rsqrtf(ss[r] * (1.f / 1024.f) + 1e-6f);
;       f32x4* orow = (f32x4*)(p.out + (size_t)(row0 + r) * 1024);
; #pragma unroll
;       for (int i = 0; i < 4; ++i) {
;         const int col = 4 * lane + 256 * i;
;         const f32x4 g4 = *(const f32x4*)(p.g_post_ffn + col), gt = *(const f32x4*)(mod + b * 6144 + 5120 + col);
;         orow[lane + 64 * i] = ov[r][i] + gt * (yv[r][i] * rstd * g4);
	v_pk_add_f32 v[172:173], v[172:173], 0 op_sel_hi:[1,0]
	v_pk_add_f32 v[172:173], v[172:173], v[174:175]
	v_pk_add_f32 v[172:173], v[172:173], v[176:177]
	v_pk_add_f32 v[172:173], v[172:173], v[178:179]
	v_pk_add_f32 v[172:173], v[172:173], v[180:181]
	v_pk_add_f32 v[172:173], v[172:173], v[182:183]
	v_pk_add_f32 v[172:173], v[172:173], v[184:185]
	v_pk_add_f32 v[172:173], v[172:173], v[186:187]
	v_pk_fma_f32 v[172:173], v[172:173], s[14:15], v[230:231]
	v_mul_f32_e32 v210, 0x4b800000, v172
	v_cmp_gt_f32_e32 vcc, s22, v172
	s_nop 1
	v_cndmask_b32_e32 v210, v172, v210, vcc
	v_rsq_f32_e32 v210, v210
	s_nop 0
	v_mul_f32_e32 v211, 0x45800000, v210
	v_cndmask_b32_e32 v226, v210, v211, vcc
	v_mul_f32_e32 v210, 0x4b800000, v173
	v_cmp_gt_f32_e32 vcc, s22, v173
	s_nop 1
	v_cndmask_b32_e32 v210, v173, v210, vcc
	v_rsq_f32_e32 v210, v210
	s_nop 0
	v_mul_f32_e32 v211, 0x45800000, v210
	v_cndmask_b32_e32 v228, v210, v211, vcc
	v_lshlrev_b32_e32 v212, 16, v156
	v_and_b32_e32 v213, 0xffff0000, v156
	v_lshlrev_b32_e32 v214, 16, v157
	v_and_b32_e32 v215, 0xffff0000, v157
	v_pk_mul_f32 v[212:213], v[226:227], v[212:213] op_sel_hi:[0,1]
	v_pk_mul_f32 v[214:215], v[226:227], v[214:215] op_sel_hi:[0,1]
	v_pk_mul_f32 v[212:213], v[212:213], v[12:13]
	v_pk_mul_f32 v[214:215], v[214:215], v[14:15]
	v_pk_fma_f32 v[124:125], v[188:189], v[212:213], v[124:125]
	v_pk_fma_f32 v[126:127], v[190:191], v[214:215], v[126:127]
	global_store_dwordx4 v2, v[124:127], s[16:17] offset:-4096
	v_lshlrev_b32_e32 v216, 16, v158
	v_and_b32_e32 v217, 0xffff0000, v158
	v_lshlrev_b32_e32 v218, 16, v159
	v_and_b32_e32 v219, 0xffff0000, v159
	v_pk_mul_f32 v[216:217], v[226:227], v[216:217] op_sel_hi:[0,1]
	v_pk_mul_f32 v[218:219], v[226:227], v[218:219] op_sel_hi:[0,1]
	v_pk_mul_f32 v[216:217], v[216:217], v[16:17]
	v_pk_mul_f32 v[218:219], v[218:219], v[18:19]
	v_pk_fma_f32 v[128:129], v[192:193], v[216:217], v[128:129]
	v_pk_fma_f32 v[130:131], v[194:195], v[218:219], v[130:131]
	global_store_dwordx4 v2, v[128:131], s[16:17] offset:-3072
	v_lshlrev_b32_e32 v212, 16, v160
	v_and_b32_e32 v213, 0xffff0000, v160
	v_lshlrev_b32_e32 v214, 16, v161
	v_and_b32_e32 v215, 0xffff0000, v161
	v_pk_mul_f32 v[212:213], v[226:227], v[212:213] op_sel_hi:[0,1]
	v_pk_mul_f32 v[214:215], v[226:227], v[214:215] op_sel_hi:[0,1]
	v_pk_mul_f32 v[212:213], v[212:213], v[20:21]
	v_pk_mul_f32 v[214:215], v[214:215], v[22:23]
	v_pk_fma_f32 v[132:133], v[196:197], v[212:213], v[132:133]
	v_pk_fma_f32 v[134:135], v[198:199], v[214:215], v[134:135]
	global_store_dwordx4 v2, v[132:135], s[16:17] offset:-2048
	v_lshlrev_b32_e32 v216, 16, v162
	v_and_b32_e32 v217, 0xffff0000, v162
	v_lshlrev_b32_e32 v218, 16, v163
	v_and_b32_e32 v219, 0xffff0000, v163
	v_pk_mul_f32 v[216:217], v[226:227], v[216:217] op_sel_hi:[0,1]
	v_pk_mul_f32 v[218:219], v[226:227], v[218:219] op_sel_hi:[0,1]
	v_pk_mul_f32 v[216:217], v[216:217], v[24:25]
	v_pk_mul_f32 v[218:219], v[218:219], v[26:27]
	v_pk_fma_f32 v[136:137], v[200:201], v[216:217], v[136:137]
	v_pk_fma_f32 v[138:139], v[202:203], v[218:219], v[138:139]
	global_store_dwordx4 v2, v[136:139], s[16:17] offset:-1024
	v_lshlrev_b32_e32 v212, 16, v164
	v_and_b32_e32 v213, 0xffff0000, v164
	v_lshlrev_b32_e32 v214, 16, v165
	v_and_b32_e32 v215, 0xffff0000, v165
	v_pk_mul_f32 v[212:213], v[228:229], v[212:213] op_sel_hi:[0,1]
	v_pk_mul_f32 v[214:215], v[228:229], v[214:215] op_sel_hi:[0,1]
	v_pk_mul_f32 v[212:213], v[212:213], v[12:13]
	v_pk_mul_f32 v[214:215], v[214:215], v[14:15]
	v_pk_fma_f32 v[140:141], v[188:189], v[212:213], v[140:141]
	v_pk_fma_f32 v[142:143], v[190:191], v[214:215], v[142:143]
	global_store_dwordx4 v2, v[140:143], s[16:17] offset:0
	v_lshlrev_b32_e32 v216, 16, v166
	v_and_b32_e32 v217, 0xffff0000, v166
	v_lshlrev_b32_e32 v218, 16, v167
	v_and_b32_e32 v219, 0xffff0000, v167
	v_pk_mul_f32 v[216:217], v[228:229], v[216:217] op_sel_hi:[0,1]
	v_pk_mul_f32 v[218:219], v[228:229], v[218:219] op_sel_hi:[0,1]
	v_pk_mul_f32 v[216:217], v[216:217], v[16:17]
	v_pk_mul_f32 v[218:219], v[218:219], v[18:19]
	v_pk_fma_f32 v[144:145], v[192:193], v[216:217], v[144:145]
	v_pk_fma_f32 v[146:147], v[194:195], v[218:219], v[146:147]
	global_store_dwordx4 v2, v[144:147], s[16:17] offset:1024
	v_lshlrev_b32_e32 v212, 16, v168
	v_and_b32_e32 v213, 0xffff0000, v168
	v_lshlrev_b32_e32 v214, 16, v169
	v_and_b32_e32 v215, 0xffff0000, v169
	v_pk_mul_f32 v[212:213], v[228:229], v[212:213] op_sel_hi:[0,1]
	v_pk_mul_f32 v[214:215], v[228:229], v[214:215] op_sel_hi:[0,1]
	v_pk_mul_f32 v[212:213], v[212:213], v[20:21]
	v_pk_mul_f32 v[214:215], v[214:215], v[22:23]
	v_pk_fma_f32 v[148:149], v[196:197], v[212:213], v[148:149]
	v_pk_fma_f32 v[150:151], v[198:199], v[214:215], v[150:151]
	global_store_dwordx4 v2, v[148:151], s[16:17] offset:2048
	v_lshlrev_b32_e32 v216, 16, v170
	v_and_b32_e32 v217, 0xffff0000, v170
	v_lshlrev_b32_e32 v218, 16, v171
	v_and_b32_e32 v219, 0xffff0000, v171
	v_pk_mul_f32 v[216:217], v[228:229], v[216:217] op_sel_hi:[0,1]
	v_pk_mul_f32 v[218:219], v[228:229], v[218:219] op_sel_hi:[0,1]
	v_pk_mul_f32 v[216:217], v[216:217], v[24:25]
	v_pk_mul_f32 v[218:219], v[218:219], v[26:27]
	v_pk_fma_f32 v[152:153], v[200:201], v[216:217], v[152:153]
	v_pk_fma_f32 v[154:155], v[202:203], v[218:219], v[154:155]
	global_store_dwordx4 v2, v[152:155], s[16:17] offset:3072
	s_add_u32 s12, s2, 0x5000
	s_lshl_b32 s13, s12, 12
	s_add_u32 s16, s66, s13
	s_addc_u32 s17, s67, 0
	s_add_u32 s16, s16, 0x1000
	s_addc_u32 s17, s17, 0
	s_lshl_b32 s13, s12, 11
	s_add_u32 s6, s84, s13
	s_addc_u32 s7, s85, 0
	s_add_u32 s6, s6, 0x6000000
	s_addc_u32 s7, s7, 0
	s_lshl_b32 s13, s12, 2
	s_add_u32 s8, s84, s13
; DI float bflo(unsigned u) { return __uint_as_float(u << 16); }
; DI float bfhi(unsigned u) { return __uint_as_float(u & 0xffff0000u); }
; DI void phase_final(const Params& p, int bid, int nb) {
;     ...
;     f32x4 ov[2][4], yv[2][4]; float ss[2] = {0.f, 0.f};
; #pragma unroll
;     for (int r = 0; r < 2; ++r) {
; #pragma unroll
;       for (int i = 0; i < 4; ++i) { ov[r][i] = ((const f32x4*)(p.out + (size_t)(row0 + r) * 1024))[lane + 64 * i];
;         const u32x2 yb = *(const u32x2*)(y2 + (size_t)(row0 + r) * 1024 + 4 * lane + 256 * i); yv[r][i] = (f32x4){bflo(yb[0]), bfhi(yb[0]), bflo(yb[1]), bfhi(yb[1])}; }
; #pragma unroll
;       for (int x = 0; x < 8; ++x) ss[r] += ssq[(size_t)x * T_ + row0 + r];
;     }
; #pragma unroll
;     for (int r = 0; r < 2; ++r) {
;       const float rstd = rsqrtf(ss[r] * (1.f / 1024.f) + 1e-6f);
;       f32x4* orow = (f32x4*)(p.out + (size_t)(row0 + r) * 1024);
; #pragma unroll
;       for (int i = 0; i < 4; ++i) {
;         const int col = 4 * lane + 256 * i;
;         const f32x4 g4 = *(const f32x4*)(p.g_post_ffn + col), gt = *(const f32x4*)(mod + b * 6144 + 5120 + col);
;         orow[lane + 64 * i] = ov[r][i] + gt * (yv[r][i] * rstd * g4);
	s_addc_u32 s9, s85, 0
	s_add_u32 s8, s8, 0x3000000
	s_addc_u32 s9, s9, 0
	s_lshr_b32 s13, s12, 13
	s_mul_i32 s13, s13, 0x6000
	s_add_u32 s10, s84, s13
	s_addc_u32 s11, s85, 0
	s_add_u32 s10, s10, 0x105000
	s_addc_u32 s11, s11, 0
	global_load_dwordx2 v[172:173], v28, s[8:9]
	global_load_dwordx2 v[174:175], v29, s[8:9]
	global_load_dwordx2 v[176:177], v30, s[8:9]
	global_load_dwordx2 v[178:179], v31, s[8:9]
	global_load_dwordx2 v[180:181], v32, s[8:9]
	global_load_dwordx2 v[182:183], v33, s[8:9]
	global_load_dwordx2 v[184:185], v34, s[8:9]
	global_load_dwordx2 v[186:187], v35, s[8:9]
	global_load_dwordx2 v[156:157], v3, s[6:7] offset:0
	global_load_dwordx2 v[158:159], v3, s[6:7] offset:512
	global_load_dwordx2 v[160:161], v3, s[6:7] offset:1024
	global_load_dwordx2 v[162:163], v3, s[6:7] offset:1536
	global_load_dwordx2 v[164:165], v3, s[6:7] offset:2048
	global_load_dwordx2 v[166:167], v3, s[6:7] offset:2560
	global_load_dwordx2 v[168:169], v3, s[6:7] offset:3072
	global_load_dwordx2 v[170:171], v3, s[6:7] offset:3584
	global_load_dwordx4 v[188:191], v2, s[10:11] offset:0
	global_load_dwordx4 v[192:195], v2, s[10:11] offset:1024
	global_load_dwordx4 v[196:199], v2, s[10:11] offset:2048
	global_load_dwordx4 v[200:203], v2, s[10:11] offset:3072
	global_load_dwordx4 v[124:127], v2, s[16:17] offset:-4096
	global_load_dwordx4 v[128:131], v2, s[16:17] offset:-3072
	global_load_dwordx4 v[132:135], v2, s[16:17] offset:-2048
	global_load_dwordx4 v[136:139], v2, s[16:17] offset:-1024
	global_load_dwordx4 v[140:143], v2, s[16:17] offset:0
	global_load_dwordx4 v[144:147], v2, s[16:17] offset:1024
	global_load_dwordx4 v[148:151], v2, s[16:17] offset:2048
	global_load_dwordx4 v[152:155], v2, s[16:17] offset:3072
	s_waitcnt vmcnt(28)
	v_pk_add_f32 v[88:89], v[88:89], 0 op_sel_hi:[1,0]
	v_pk_add_f32 v[88:89], v[88:89], v[90:91]
	v_pk_add_f32 v[88:89], v[88:89], v[92:93]
	v_pk_add_f32 v[88:89], v[88:89], v[94:95]
	v_pk_add_f32 v[88:89], v[88:89], v[96:97]
	v_pk_add_f32 v[88:89], v[88:89], v[98:99]
	v_pk_add_f32 v[88:89], v[88:89], v[100:101]
	v_pk_add_f32 v[88:89], v[88:89], v[102:103]
	v_pk_fma_f32 v[88:89], v[88:89], s[14:15], v[230:231]
	v_mul_f32_e32 v210, 0x4b800000, v88
	v_cmp_gt_f32_e32 vcc, s22, v88
	s_nop 1
	v_cndmask_b32_e32 v210, v88, v210, vcc
	v_rsq_f32_e32 v210, v210
	s_nop 0
	v_mul_f32_e32 v211, 0x45800000, v210
	v_cndmask_b32_e32 v226, v210, v211, vcc
	v_mul_f32_e32 v210, 0x4b800000, v89
	v_cmp_gt_f32_e32 vcc, s22, v89
	s_nop 1
	v_cndmask_b32_e32 v210, v89, v210, vcc
	v_rsq_f32_e32 v210, v210
	s_nop 0
	v_mul_f32_e32 v211, 0x45800000, v210
	v_cndmask_b32_e32 v228, v210, v211, vcc
	v_lshlrev_b32_e32 v212, 16, v72
	v_and_b32_e32 v213, 0xffff0000, v72
	v_lshlrev_b32_e32 v214, 16, v73
	v_and_b32_e32 v215, 0xffff0000, v73
	v_pk_mul_f32 v[212:213], v[226:227], v[212:213] op_sel_hi:[0,1]
	v_pk_mul_f32 v[214:215], v[226:227], v[214:215] op_sel_hi:[0,1]
	v_pk_mul_f32 v[212:213], v[212:213], v[12:13]
	v_pk_mul_f32 v[214:215], v[214:215], v[14:15]
	v_pk_fma_f32 v[40:41], v[104:105], v[212:213], v[40:41]
	v_pk_fma_f32 v[42:43], v[106:107], v[214:215], v[42:43]
	global_store_dwordx4 v2, v[40:43], s[4:5] offset:-4096
	v_lshlrev_b32_e32 v216, 16, v74
	v_and_b32_e32 v217, 0xffff0000, v74
	v_lshlrev_b32_e32 v218, 16, v75
	v_and_b32_e32 v219, 0xffff0000, v75
	v_pk_mul_f32 v[216:217], v[226:227], v[216:217] op_sel_hi:[0,1]
	v_pk_mul_f32 v[218:219], v[226:227], v[218:219] op_sel_hi:[0,1]
	v_pk_mul_f32 v[216:217], v[216:217], v[16:17]
	v_pk_mul_f32 v[218:219], v[218:219], v[18:19]
	v_pk_fma_f32 v[44:45], v[108:109], v[216:217], v[44:45]
	v_pk_fma_f32 v[46:47], v[110:111], v[218:219], v[46:47]
	global_store_dwordx4 v2, v[44:47], s[4:5] offset:-3072
	v_lshlrev_b32_e32 v212, 16, v76
	v_and_b32_e32 v213, 0xffff0000, v76
	v_lshlrev_b32_e32 v214, 16, v77
	v_and_b32_e32 v215, 0xffff0000, v77
	v_pk_mul_f32 v[212:213], v[226:227], v[212:213] op_sel_hi:[0,1]
	v_pk_mul_f32 v[214:215], v[226:227], v[214:215] op_sel_hi:[0,1]
	v_pk_mul_f32 v[212:213], v[212:213], v[20:21]
	v_pk_mul_f32 v[214:215], v[214:215], v[22:23]
	v_pk_fma_f32 v[48:49], v[112:113], v[212:213], v[48:49]
	v_pk_fma_f32 v[50:51], v[114:115], v[214:215], v[50:51]
	global_store_dwordx4 v2, v[48:51], s[4:5] offset:-2048
	v_lshlrev_b32_e32 v216, 16, v78
	v_and_b32_e32 v217, 0xffff0000, v78
	v_lshlrev_b32_e32 v218, 16, v79
	v_and_b32_e32 v219, 0xffff0000, v79
	v_pk_mul_f32 v[216:217], v[226:227], v[216:217] op_sel_hi:[0,1]
	v_pk_mul_f32 v[218:219], v[226:227], v[218:219] op_sel_hi:[0,1]
	v_pk_mul_f32 v[216:217], v[216:217], v[24:25]
	v_pk_mul_f32 v[218:219], v[218:219], v[26:27]
	v_pk_fma_f32 v[52:53], v[116:117], v[216:217], v[52:53]
	v_pk_fma_f32 v[54:55], v[118:119], v[218:219], v[54:55]
	global_store_dwordx4 v2, v[52:55], s[4:5] offset:-1024
	v_lshlrev_b32_e32 v212, 16, v80
	v_and_b32_e32 v213, 0xffff0000, v80
	v_lshlrev_b32_e32 v214, 16, v81
	v_and_b32_e32 v215, 0xffff0000, v81
	v_pk_mul_f32 v[212:213], v[228:229], v[212:213] op_sel_hi:[0,1]
	v_pk_mul_f32 v[214:215], v[228:229], v[214:215] op_sel_hi:[0,1]
	v_pk_mul_f32 v[212:213], v[212:213], v[12:13]
	v_pk_mul_f32 v[214:215], v[214:215], v[14:15]
	v_pk_fma_f32 v[56:57], v[104:105], v[212:213], v[56:57]
	v_pk_fma_f32 v[58:59], v[106:107], v[214:215], v[58:59]
	global_store_dwordx4 v2, v[56:59], s[4:5] offset:0
	v_lshlrev_b32_e32 v216, 16, v82
	v_and_b32_e32 v217, 0xffff0000, v82
	v_lshlrev_b32_e32 v218, 16, v83
	v_and_b32_e32 v219, 0xffff0000, v83
	v_pk_mul_f32 v[216:217], v[228:229], v[216:217] op_sel_hi:[0,1]
	v_pk_mul_f32 v[218:219], v[228:229], v[218:219] op_sel_hi:[0,1]
	v_pk_mul_f32 v[216:217], v[216:217], v[16:17]
	v_pk_mul_f32 v[218:219], v[218:219], v[18:19]
; DI float bflo(unsigned u) { return __uint_as_float(u << 16); }
; DI float bfhi(unsigned u) { return __uint_as_float(u & 0xffff0000u); }
; DI void phase_final(const Params& p, int bid, int nb) {
;     ...
;     f32x4 ov[2][4], yv[2][4]; float ss[2] = {0.f, 0.f};
; #pragma unroll
;     for (int r = 0; r < 2; ++r) {
; #pragma unroll
;       for (int i = 0; i < 4; ++i) { ov[r][i] = ((const f32x4*)(p.out + (size_t)(row0 + r) * 1024))[lane + 64 * i];
;         const u32x2 yb = *(const u32x2*)(y2 + (size_t)(row0 + r) * 1024 + 4 * lane + 256 * i); yv[r][i] = (f32x4){bflo(yb[0]), bfhi(yb[0]), bflo(yb[1]), bfhi(yb[1])}; }
; #pragma unroll
;       for (int x = 0; x < 8; ++x) ss[r] += ssq[(size_t)x * T_ + row0 + r];
;     }
; #pragma unroll
;     for (int r = 0; r < 2; ++r) {
;       const float rstd = rsqrtf(ss[r] * (1.f / 1024.f) + 1e-6f);
;       f32x4* orow = (f32x4*)(p.out + (size_t)(row0 + r) * 1024);
; #pragma unroll
;       for (int i = 0; i < 4; ++i) {
;         const int col = 4 * lane + 256 * i;
;         const f32x4 g4 = *(const f32x4*)(p.g_post_ffn + col), gt = *(const f32x4*)(mod + b * 6144 + 5120 + col);
;         orow[lane + 64 * i] = ov[r][i] + gt * (yv[r][i] * rstd * g4);
	v_pk_fma_f32 v[60:61], v[108:109], v[216:217], v[60:61]
	v_pk_fma_f32 v[62:63], v[110:111], v[218:219], v[62:63]
	global_store_dwordx4 v2, v[60:63], s[4:5] offset:1024
	v_lshlrev_b32_e32 v212, 16, v84
	v_and_b32_e32 v213, 0xffff0000, v84
	v_lshlrev_b32_e32 v214, 16, v85
	v_and_b32_e32 v215, 0xffff0000, v85
	v_pk_mul_f32 v[212:213], v[228:229], v[212:213] op_sel_hi:[0,1]
	v_pk_mul_f32 v[214:215], v[228:229], v[214:215] op_sel_hi:[0,1]
	v_pk_mul_f32 v[212:213], v[212:213], v[20:21]
	v_pk_mul_f32 v[214:215], v[214:215], v[22:23]
	v_pk_fma_f32 v[64:65], v[112:113], v[212:213], v[64:65]
	v_pk_fma_f32 v[66:67], v[114:115], v[214:215], v[66:67]
	global_store_dwordx4 v2, v[64:67], s[4:5] offset:2048
	v_lshlrev_b32_e32 v216, 16, v86
	v_and_b32_e32 v217, 0xffff0000, v86
	v_lshlrev_b32_e32 v218, 16, v87
	v_and_b32_e32 v219, 0xffff0000, v87
	v_pk_mul_f32 v[216:217], v[228:229], v[216:217] op_sel_hi:[0,1]
	v_pk_mul_f32 v[218:219], v[228:229], v[218:219] op_sel_hi:[0,1]
	v_pk_mul_f32 v[216:217], v[216:217], v[24:25]
	v_pk_mul_f32 v[218:219], v[218:219], v[26:27]
	v_pk_fma_f32 v[68:69], v[116:117], v[216:217], v[68:69]
	v_pk_fma_f32 v[70:71], v[118:119], v[218:219], v[70:71]
	global_store_dwordx4 v2, v[68:71], s[4:5] offset:3072
	s_add_u32 s12, s2, 0x6000
	s_lshl_b32 s13, s12, 12
	s_add_u32 s4, s66, s13
	s_addc_u32 s5, s67, 0
	s_add_u32 s4, s4, 0x1000
	s_addc_u32 s5, s5, 0
	s_lshl_b32 s13, s12, 11
	s_add_u32 s6, s84, s13
	s_addc_u32 s7, s85, 0
	s_add_u32 s6, s6, 0x6000000
	s_addc_u32 s7, s7, 0
	s_lshl_b32 s13, s12, 2
	s_add_u32 s8, s84, s13
	s_addc_u32 s9, s85, 0
	s_add_u32 s8, s8, 0x3000000
	s_addc_u32 s9, s9, 0
	s_lshr_b32 s13, s12, 13
	s_mul_i32 s13, s13, 0x6000
	s_add_u32 s10, s84, s13
	s_addc_u32 s11, s85, 0
	s_add_u32 s10, s10, 0x105000
	s_addc_u32 s11, s11, 0
	global_load_dwordx2 v[88:89], v28, s[8:9]
	global_load_dwordx2 v[90:91], v29, s[8:9]
	global_load_dwordx2 v[92:93], v30, s[8:9]
	global_load_dwordx2 v[94:95], v31, s[8:9]
	global_load_dwordx2 v[96:97], v32, s[8:9]
	global_load_dwordx2 v[98:99], v33, s[8:9]
	global_load_dwordx2 v[100:101], v34, s[8:9]
	global_load_dwordx2 v[102:103], v35, s[8:9]
	global_load_dwordx2 v[72:73], v3, s[6:7] offset:0
	global_load_dwordx2 v[74:75], v3, s[6:7] offset:512
	global_load_dwordx2 v[76:77], v3, s[6:7] offset:1024
	global_load_dwordx2 v[78:79], v3, s[6:7] offset:1536
	global_load_dwordx2 v[80:81], v3, s[6:7] offset:2048
	global_load_dwordx2 v[82:83], v3, s[6:7] offset:2560
	global_load_dwordx2 v[84:85], v3, s[6:7] offset:3072
	global_load_dwordx2 v[86:87], v3, s[6:7] offset:3584
	global_load_dwordx4 v[104:107], v2, s[10:11] offset:0
	global_load_dwordx4 v[108:111], v2, s[10:11] offset:1024
	global_load_dwordx4 v[112:115], v2, s[10:11] offset:2048
	global_load_dwordx4 v[116:119], v2, s[10:11] offset:3072
	global_load_dwordx4 v[40:43], v2, s[4:5] offset:-4096
	global_load_dwordx4 v[44:47], v2, s[4:5] offset:-3072
	global_load_dwordx4 v[48:51], v2, s[4:5] offset:-2048
	global_load_dwordx4 v[52:55], v2, s[4:5] offset:-1024
	global_load_dwordx4 v[56:59], v2, s[4:5] offset:0
	global_load_dwordx4 v[60:63], v2, s[4:5] offset:1024
	global_load_dwordx4 v[64:67], v2, s[4:5] offset:2048
	global_load_dwordx4 v[68:71], v2, s[4:5] offset:3072
	s_waitcnt vmcnt(28)
	v_pk_add_f32 v[172:173], v[172:173], 0 op_sel_hi:[1,0]
	v_pk_add_f32 v[172:173], v[172:173], v[174:175]
	v_pk_add_f32 v[172:173], v[172:173], v[176:177]
	v_pk_add_f32 v[172:173], v[172:173], v[178:179]
	v_pk_add_f32 v[172:173], v[172:173], v[180:181]
	v_pk_add_f32 v[172:173], v[172:173], v[182:183]
	v_pk_add_f32 v[172:173], v[172:173], v[184:185]
	v_pk_add_f32 v[172:173], v[172:173], v[186:187]
	v_pk_fma_f32 v[172:173], v[172:173], s[14:15], v[230:231]
	v_mul_f32_e32 v210, 0x4b800000, v172
	v_cmp_gt_f32_e32 vcc, s22, v172
	s_nop 1
	v_cndmask_b32_e32 v210, v172, v210, vcc
	v_rsq_f32_e32 v210, v210
	s_nop 0
	v_mul_f32_e32 v211, 0x45800000, v210
	v_cndmask_b32_e32 v226, v210, v211, vcc
	v_mul_f32_e32 v210, 0x4b800000, v173
	v_cmp_gt_f32_e32 vcc, s22, v173
	s_nop 1
	v_cndmask_b32_e32 v210, v173, v210, vcc
	v_rsq_f32_e32 v210, v210
	s_nop 0
	v_mul_f32_e32 v211, 0x45800000, v210
	v_cndmask_b32_e32 v228, v210, v211, vcc
	v_lshlrev_b32_e32 v212, 16, v156
	v_and_b32_e32 v213, 0xffff0000, v156
	v_lshlrev_b32_e32 v214, 16, v157
	v_and_b32_e32 v215, 0xffff0000, v157
	v_pk_mul_f32 v[212:213], v[226:227], v[212:213] op_sel_hi:[0,1]
	v_pk_mul_f32 v[214:215], v[226:227], v[214:215] op_sel_hi:[0,1]
	v_pk_mul_f32 v[212:213], v[212:213], v[12:13]
	v_pk_mul_f32 v[214:215], v[214:215], v[14:15]
	v_pk_fma_f32 v[124:125], v[188:189], v[212:213], v[124:125]
	v_pk_fma_f32 v[126:127], v[190:191], v[214:215], v[126:127]
	global_store_dwordx4 v2, v[124:127], s[16:17] offset:-4096
	v_lshlrev_b32_e32 v216, 16, v158
	v_and_b32_e32 v217, 0xffff0000, v158
	v_lshlrev_b32_e32 v218, 16, v159
	v_and_b32_e32 v219, 0xffff0000, v159
	v_pk_mul_f32 v[216:217], v[226:227], v[216:217] op_sel_hi:[0,1]
	v_pk_mul_f32 v[218:219], v[226:227], v[218:219] op_sel_hi:[0,1]
	v_pk_mul_f32 v[216:217], v[216:217], v[16:17]
	v_pk_mul_f32 v[218:219], v[218:219], v[18:19]
	v_pk_fma_f32 v[128:129], v[192:193], v[216:217], v[128:129]
	v_pk_fma_f32 v[130:131], v[194:195], v[218:219], v[130:131]
	global_store_dwordx4 v2, v[128:131], s[16:17] offset:-3072
	v_lshlrev_b32_e32 v212, 16, v160
	v_and_b32_e32 v213, 0xffff0000, v160
	v_lshlrev_b32_e32 v214, 16, v161
	v_and_b32_e32 v215, 0xffff0000, v161
	v_pk_mul_f32 v[212:213], v[226:227], v[212:213] op_sel_hi:[0,1]
	v_pk_mul_f32 v[214:215], v[226:227], v[214:215] op_sel_hi:[0,1]
	v_pk_mul_f32 v[212:213], v[212:213], v[20:21]
	v_pk_mul_f32 v[214:215], v[214:215], v[22:23]
; DI float bflo(unsigned u) { return __uint_as_float(u << 16); }
; DI float bfhi(unsigned u) { return __uint_as_float(u & 0xffff0000u); }
; DI void phase_final(const Params& p, int bid, int nb) {
;     ...
;     f32x4 ov[2][4], yv[2][4]; float ss[2] = {0.f, 0.f};
; #pragma unroll
;     for (int r = 0; r < 2; ++r) {
; #pragma unroll
;       for (int i = 0; i < 4; ++i) { ov[r][i] = ((const f32x4*)(p.out + (size_t)(row0 + r) * 1024))[lane + 64 * i];
;         const u32x2 yb = *(const u32x2*)(y2 + (size_t)(row0 + r) * 1024 + 4 * lane + 256 * i); yv[r][i] = (f32x4){bflo(yb[0]), bfhi(yb[0]), bflo(yb[1]), bfhi(yb[1])}; }
; #pragma unroll
;       for (int x = 0; x < 8; ++x) ss[r] += ssq[(size_t)x * T_ + row0 + r];
;     }
; #pragma unroll
;     for (int r = 0; r < 2; ++r) {
;       const float rstd = rsqrtf(ss[r] * (1.f / 1024.f) + 1e-6f);
;       f32x4* orow = (f32x4*)(p.out + (size_t)(row0 + r) * 1024);
; #pragma unroll
;       for (int i = 0; i < 4; ++i) {
;         const int col = 4 * lane + 256 * i;
;         const f32x4 g4 = *(const f32x4*)(p.g_post_ffn + col), gt = *(const f32x4*)(mod + b * 6144 + 5120 + col);
;         orow[lane + 64 * i] = ov[r][i] + gt * (yv[r][i] * rstd * g4);
	v_pk_fma_f32 v[132:133], v[196:197], v[212:213], v[132:133]
	v_pk_fma_f32 v[134:135], v[198:199], v[214:215], v[134:135]
	global_store_dwordx4 v2, v[132:135], s[16:17] offset:-2048
	v_lshlrev_b32_e32 v216, 16, v162
	v_and_b32_e32 v217, 0xffff0000, v162
	v_lshlrev_b32_e32 v218, 16, v163
	v_and_b32_e32 v219, 0xffff0000, v163
	v_pk_mul_f32 v[216:217], v[226:227], v[216:217] op_sel_hi:[0,1]
	v_pk_mul_f32 v[218:219], v[226:227], v[218:219] op_sel_hi:[0,1]
	v_pk_mul_f32 v[216:217], v[216:217], v[24:25]
	v_pk_mul_f32 v[218:219], v[218:219], v[26:27]
	v_pk_fma_f32 v[136:137], v[200:201], v[216:217], v[136:137]
	v_pk_fma_f32 v[138:139], v[202:203], v[218:219], v[138:139]
	global_store_dwordx4 v2, v[136:139], s[16:17] offset:-1024
	v_lshlrev_b32_e32 v212, 16, v164
	v_and_b32_e32 v213, 0xffff0000, v164
	v_lshlrev_b32_e32 v214, 16, v165
	v_and_b32_e32 v215, 0xffff0000, v165
	v_pk_mul_f32 v[212:213], v[228:229], v[212:213] op_sel_hi:[0,1]
	v_pk_mul_f32 v[214:215], v[228:229], v[214:215] op_sel_hi:[0,1]
	v_pk_mul_f32 v[212:213], v[212:213], v[12:13]
	v_pk_mul_f32 v[214:215], v[214:215], v[14:15]
	v_pk_fma_f32 v[140:141], v[188:189], v[212:213], v[140:141]
	v_pk_fma_f32 v[142:143], v[190:191], v[214:215], v[142:143]
	global_store_dwordx4 v2, v[140:143], s[16:17] offset:0
	v_lshlrev_b32_e32 v216, 16, v166
	v_and_b32_e32 v217, 0xffff0000, v166
	v_lshlrev_b32_e32 v218, 16, v167
	v_and_b32_e32 v219, 0xffff0000, v167
	v_pk_mul_f32 v[216:217], v[228:229], v[216:217] op_sel_hi:[0,1]
	v_pk_mul_f32 v[218:219], v[228:229], v[218:219] op_sel_hi:[0,1]
	v_pk_mul_f32 v[216:217], v[216:217], v[16:17]
	v_pk_mul_f32 v[218:219], v[218:219], v[18:19]
	v_pk_fma_f32 v[144:145], v[192:193], v[216:217], v[144:145]
	v_pk_fma_f32 v[146:147], v[194:195], v[218:219], v[146:147]
	global_store_dwordx4 v2, v[144:147], s[16:17] offset:1024
	v_lshlrev_b32_e32 v212, 16, v168
	v_and_b32_e32 v213, 0xffff0000, v168
	v_lshlrev_b32_e32 v214, 16, v169
	v_and_b32_e32 v215, 0xffff0000, v169
	v_pk_mul_f32 v[212:213], v[228:229], v[212:213] op_sel_hi:[0,1]
	v_pk_mul_f32 v[214:215], v[228:229], v[214:215] op_sel_hi:[0,1]
	v_pk_mul_f32 v[212:213], v[212:213], v[20:21]
	v_pk_mul_f32 v[214:215], v[214:215], v[22:23]
	v_pk_fma_f32 v[148:149], v[196:197], v[212:213], v[148:149]
	v_pk_fma_f32 v[150:151], v[198:199], v[214:215], v[150:151]
	global_store_dwordx4 v2, v[148:151], s[16:17] offset:2048
	v_lshlrev_b32_e32 v216, 16, v170
	v_and_b32_e32 v217, 0xffff0000, v170
	v_lshlrev_b32_e32 v218, 16, v171
	v_and_b32_e32 v219, 0xffff0000, v171
	v_pk_mul_f32 v[216:217], v[228:229], v[216:217] op_sel_hi:[0,1]
	v_pk_mul_f32 v[218:219], v[228:229], v[218:219] op_sel_hi:[0,1]
	v_pk_mul_f32 v[216:217], v[216:217], v[24:25]
	v_pk_mul_f32 v[218:219], v[218:219], v[26:27]
	v_pk_fma_f32 v[152:153], v[200:201], v[216:217], v[152:153]
	v_pk_fma_f32 v[154:155], v[202:203], v[218:219], v[154:155]
	global_store_dwordx4 v2, v[152:155], s[16:17] offset:3072
	s_add_u32 s12, s2, 0x7000
	s_lshl_b32 s13, s12, 12
	s_add_u32 s16, s66, s13
	s_addc_u32 s17, s67, 0
	s_add_u32 s16, s16, 0x1000
	s_addc_u32 s17, s17, 0
	s_lshl_b32 s13, s12, 11
	s_add_u32 s6, s84, s13
	s_addc_u32 s7, s85, 0
	s_add_u32 s6, s6, 0x6000000
	s_addc_u32 s7, s7, 0
	s_lshl_b32 s13, s12, 2
	s_add_u32 s8, s84, s13
	s_addc_u32 s9, s85, 0
	s_add_u32 s8, s8, 0x3000000
	s_addc_u32 s9, s9, 0
	s_lshr_b32 s13, s12, 13
	s_mul_i32 s13, s13, 0x6000
	s_add_u32 s10, s84, s13
	s_addc_u32 s11, s85, 0
	s_add_u32 s10, s10, 0x105000
	s_addc_u32 s11, s11, 0
	global_load_dwordx2 v[172:173], v28, s[8:9]
	global_load_dwordx2 v[174:175], v29, s[8:9]
	global_load_dwordx2 v[176:177], v30, s[8:9]
	global_load_dwordx2 v[178:179], v31, s[8:9]
	global_load_dwordx2 v[180:181], v32, s[8:9]
	global_load_dwordx2 v[182:183], v33, s[8:9]
	global_load_dwordx2 v[184:185], v34, s[8:9]
	global_load_dwordx2 v[186:187], v35, s[8:9]
	global_load_dwordx2 v[156:157], v3, s[6:7] offset:0
	global_load_dwordx2 v[158:159], v3, s[6:7] offset:512
	global_load_dwordx2 v[160:161], v3, s[6:7] offset:1024
	global_load_dwordx2 v[162:163], v3, s[6:7] offset:1536
	global_load_dwordx2 v[164:165], v3, s[6:7] offset:2048
	global_load_dwordx2 v[166:167], v3, s[6:7] offset:2560
	global_load_dwordx2 v[168:169], v3, s[6:7] offset:3072
	global_load_dwordx2 v[170:171], v3, s[6:7] offset:3584
	global_load_dwordx4 v[188:191], v2, s[10:11] offset:0
	global_load_dwordx4 v[192:195], v2, s[10:11] offset:1024
	global_load_dwordx4 v[196:199], v2, s[10:11] offset:2048
	global_load_dwordx4 v[200:203], v2, s[10:11] offset:3072
	global_load_dwordx4 v[124:127], v2, s[16:17] offset:-4096
	global_load_dwordx4 v[128:131], v2, s[16:17] offset:-3072
	global_load_dwordx4 v[132:135], v2, s[16:17] offset:-2048
	global_load_dwordx4 v[136:139], v2, s[16:17] offset:-1024
	global_load_dwordx4 v[140:143], v2, s[16:17] offset:0
	global_load_dwordx4 v[144:147], v2, s[16:17] offset:1024
	global_load_dwordx4 v[148:151], v2, s[16:17] offset:2048
	global_load_dwordx4 v[152:155], v2, s[16:17] offset:3072
	s_waitcnt vmcnt(28)
; DI float bflo(unsigned u) { return __uint_as_float(u << 16); }
; DI float bfhi(unsigned u) { return __uint_as_float(u & 0xffff0000u); }
; DI void phase_final(const Params& p, int bid, int nb) {
;     ...
;     f32x4 ov[2][4], yv[2][4]; float ss[2] = {0.f, 0.f};
; #pragma unroll
;     for (int r = 0; r < 2; ++r) {
; #pragma unroll
;       for (int i = 0; i < 4; ++i) { ov[r][i] = ((const f32x4*)(p.out + (size_t)(row0 + r) * 1024))[lane + 64 * i];
;         const u32x2 yb = *(const u32x2*)(y2 + (size_t)(row0 + r) * 1024 + 4 * lane + 256 * i); yv[r][i] = (f32x4){bflo(yb[0]), bfhi(yb[0]), bflo(yb[1]), bfhi(yb[1])}; }
; #pragma unroll
;       for (int x = 0; x < 8; ++x) ss[r] += ssq[(size_t)x * T_ + row0 + r];
;     }
; #pragma unroll
;     for (int r = 0; r < 2; ++r) {
;       const float rstd = rsqrtf(ss[r] * (1.f / 1024.f) + 1e-6f);
;       f32x4* orow = (f32x4*)(p.out + (size_t)(row0 + r) * 1024);
; #pragma unroll
;       for (int i = 0; i < 4; ++i) {
;         const int col = 4 * lane + 256 * i;
;         const f32x4 g4 = *(const f32x4*)(p.g_post_ffn + col), gt = *(const f32x4*)(mod + b * 6144 + 5120 + col);
;         orow[lane + 64 * i] = ov[r][i] + gt * (yv[r][i] * rstd * g4);
	v_pk_add_f32 v[88:89], v[88:89], 0 op_sel_hi:[1,0]
	v_pk_add_f32 v[88:89], v[88:89], v[90:91]
	v_pk_add_f32 v[88:89], v[88:89], v[92:93]
	v_pk_add_f32 v[88:89], v[88:89], v[94:95]
	v_pk_add_f32 v[88:89], v[88:89], v[96:97]
	v_pk_add_f32 v[88:89], v[88:89], v[98:99]
	v_pk_add_f32 v[88:89], v[88:89], v[100:101]
	v_pk_add_f32 v[88:89], v[88:89], v[102:103]
	v_pk_fma_f32 v[88:89], v[88:89], s[14:15], v[230:231]
	v_mul_f32_e32 v210, 0x4b800000, v88
	v_cmp_gt_f32_e32 vcc, s22, v88
	s_nop 1
	v_cndmask_b32_e32 v210, v88, v210, vcc
	v_rsq_f32_e32 v210, v210
	s_nop 0
	v_mul_f32_e32 v211, 0x45800000, v210
	v_cndmask_b32_e32 v226, v210, v211, vcc
	v_mul_f32_e32 v210, 0x4b800000, v89
	v_cmp_gt_f32_e32 vcc, s22, v89
	s_nop 1
	v_cndmask_b32_e32 v210, v89, v210, vcc
	v_rsq_f32_e32 v210, v210
	s_nop 0
	v_mul_f32_e32 v211, 0x45800000, v210
	v_cndmask_b32_e32 v228, v210, v211, vcc
	v_lshlrev_b32_e32 v212, 16, v72
	v_and_b32_e32 v213, 0xffff0000, v72
	v_lshlrev_b32_e32 v214, 16, v73
	v_and_b32_e32 v215, 0xffff0000, v73
	v_pk_mul_f32 v[212:213], v[226:227], v[212:213] op_sel_hi:[0,1]
	v_pk_mul_f32 v[214:215], v[226:227], v[214:215] op_sel_hi:[0,1]
	v_pk_mul_f32 v[212:213], v[212:213], v[12:13]
	v_pk_mul_f32 v[214:215], v[214:215], v[14:15]
	v_pk_fma_f32 v[40:41], v[104:105], v[212:213], v[40:41]
	v_pk_fma_f32 v[42:43], v[106:107], v[214:215], v[42:43]
	global_store_dwordx4 v2, v[40:43], s[4:5] offset:-4096
	v_lshlrev_b32_e32 v216, 16, v74
	v_and_b32_e32 v217, 0xffff0000, v74
	v_lshlrev_b32_e32 v218, 16, v75
	v_and_b32_e32 v219, 0xffff0000, v75
	v_pk_mul_f32 v[216:217], v[226:227], v[216:217] op_sel_hi:[0,1]
	v_pk_mul_f32 v[218:219], v[226:227], v[218:219] op_sel_hi:[0,1]
	v_pk_mul_f32 v[216:217], v[216:217], v[16:17]
	v_pk_mul_f32 v[218:219], v[218:219], v[18:19]
	v_pk_fma_f32 v[44:45], v[108:109], v[216:217], v[44:45]
	v_pk_fma_f32 v[46:47], v[110:111], v[218:219], v[46:47]
	global_store_dwordx4 v2, v[44:47], s[4:5] offset:-3072
	v_lshlrev_b32_e32 v212, 16, v76
	v_and_b32_e32 v213, 0xffff0000, v76
	v_lshlrev_b32_e32 v214, 16, v77
	v_and_b32_e32 v215, 0xffff0000, v77
	v_pk_mul_f32 v[212:213], v[226:227], v[212:213] op_sel_hi:[0,1]
	v_pk_mul_f32 v[214:215], v[226:227], v[214:215] op_sel_hi:[0,1]
	v_pk_mul_f32 v[212:213], v[212:213], v[20:21]
	v_pk_mul_f32 v[214:215], v[214:215], v[22:23]
	v_pk_fma_f32 v[48:49], v[112:113], v[212:213], v[48:49]
	v_pk_fma_f32 v[50:51], v[114:115], v[214:215], v[50:51]
	global_store_dwordx4 v2, v[48:51], s[4:5] offset:-2048
	v_lshlrev_b32_e32 v216, 16, v78
	v_and_b32_e32 v217, 0xffff0000, v78
	v_lshlrev_b32_e32 v218, 16, v79
	v_and_b32_e32 v219, 0xffff0000, v79
	v_pk_mul_f32 v[216:217], v[226:227], v[216:217] op_sel_hi:[0,1]
	v_pk_mul_f32 v[218:219], v[226:227], v[218:219] op_sel_hi:[0,1]
	v_pk_mul_f32 v[216:217], v[216:217], v[24:25]
	v_pk_mul_f32 v[218:219], v[218:219], v[26:27]
	v_pk_fma_f32 v[52:53], v[116:117], v[216:217], v[52:53]
	v_pk_fma_f32 v[54:55], v[118:119], v[218:219], v[54:55]
	global_store_dwordx4 v2, v[52:55], s[4:5] offset:-1024
	v_lshlrev_b32_e32 v212, 16, v80
	v_and_b32_e32 v213, 0xffff0000, v80
	v_lshlrev_b32_e32 v214, 16, v81
	v_and_b32_e32 v215, 0xffff0000, v81
	v_pk_mul_f32 v[212:213], v[228:229], v[212:213] op_sel_hi:[0,1]
	v_pk_mul_f32 v[214:215], v[228:229], v[214:215] op_sel_hi:[0,1]
	v_pk_mul_f32 v[212:213], v[212:213], v[12:13]
	v_pk_mul_f32 v[214:215], v[214:215], v[14:15]
	v_pk_fma_f32 v[56:57], v[104:105], v[212:213], v[56:57]
	v_pk_fma_f32 v[58:59], v[106:107], v[214:215], v[58:59]
	global_store_dwordx4 v2, v[56:59], s[4:5] offset:0
	v_lshlrev_b32_e32 v216, 16, v82
	v_and_b32_e32 v217, 0xffff0000, v82
	v_lshlrev_b32_e32 v218, 16, v83
	v_and_b32_e32 v219, 0xffff0000, v83
	v_pk_mul_f32 v[216:217], v[228:229], v[216:217] op_sel_hi:[0,1]
	v_pk_mul_f32 v[218:219], v[228:229], v[218:219] op_sel_hi:[0,1]
	v_pk_mul_f32 v[216:217], v[216:217], v[16:17]
	v_pk_mul_f32 v[218:219], v[218:219], v[18:19]
	v_pk_fma_f32 v[60:61], v[108:109], v[216:217], v[60:61]
	v_pk_fma_f32 v[62:63], v[110:111], v[218:219], v[62:63]
	global_store_dwordx4 v2, v[60:63], s[4:5] offset:1024
	v_lshlrev_b32_e32 v212, 16, v84
	v_and_b32_e32 v213, 0xffff0000, v84
	v_lshlrev_b32_e32 v214, 16, v85
	v_and_b32_e32 v215, 0xffff0000, v85
	v_pk_mul_f32 v[212:213], v[228:229], v[212:213] op_sel_hi:[0,1]
	v_pk_mul_f32 v[214:215], v[228:229], v[214:215] op_sel_hi:[0,1]
	v_pk_mul_f32 v[212:213], v[212:213], v[20:21]
	v_pk_mul_f32 v[214:215], v[214:215], v[22:23]
	v_pk_fma_f32 v[64:65], v[112:113], v[212:213], v[64:65]
	v_pk_fma_f32 v[66:67], v[114:115], v[214:215], v[66:67]
	global_store_dwordx4 v2, v[64:67], s[4:5] offset:2048
	v_lshlrev_b32_e32 v216, 16, v86
	v_and_b32_e32 v217, 0xffff0000, v86
	v_lshlrev_b32_e32 v218, 16, v87
	v_and_b32_e32 v219, 0xffff0000, v87
	v_pk_mul_f32 v[216:217], v[228:229], v[216:217] op_sel_hi:[0,1]
	v_pk_mul_f32 v[218:219], v[228:229], v[218:219] op_sel_hi:[0,1]
	v_pk_mul_f32 v[216:217], v[216:217], v[24:25]
	v_pk_mul_f32 v[218:219], v[218:219], v[26:27]
	v_pk_fma_f32 v[68:69], v[116:117], v[216:217], v[68:69]
	v_pk_fma_f32 v[70:71], v[118:119], v[218:219], v[70:71]
	global_store_dwordx4 v2, v[68:71], s[4:5] offset:3072
	s_waitcnt vmcnt(0)
; DI void phase_final(const Params& p, int bid, int nb) {
;     ...
;       for (int x = 0; x < 8; ++x) ss[r] += ssq[(size_t)x * T_ + row0 + r];
;     }
; #pragma unroll
;     for (int r = 0; r < 2; ++r) {
;       const float rstd = rsqrtf(ss[r] * (1.f / 1024.f) + 1e-6f);
;       f32x4* orow = (f32x4*)(p.out + (size_t)(row0 + r) * 1024);
; #pragma unroll
;       for (int i = 0; i < 4; ++i) {
;         const int col = 4 * lane + 256 * i;
;         const f32x4 g4 = *(const f32x4*)(p.g_post_ffn + col), gt = *(const f32x4*)(mod + b * 6144 + 5120 + col);
;         orow[lane + 64 * i] = ov[r][i] + gt * (yv[r][i] * rstd * g4);
;       }
;     }
	v_pk_add_f32 v[172:173], v[172:173], 0 op_sel_hi:[1,0]
	v_pk_add_f32 v[172:173], v[172:173], v[174:175]
	v_pk_add_f32 v[172:173], v[172:173], v[176:177]
	v_pk_add_f32 v[172:173], v[172:173], v[178:179]
	v_pk_add_f32 v[172:173], v[172:173], v[180:181]
	v_pk_add_f32 v[172:173], v[172:173], v[182:183]
	v_pk_add_f32 v[172:173], v[172:173], v[184:185]
	v_pk_add_f32 v[172:173], v[172:173], v[186:187]
	v_pk_fma_f32 v[172:173], v[172:173], s[14:15], v[230:231]
	v_mul_f32_e32 v210, 0x4b800000, v172
	v_cmp_gt_f32_e32 vcc, s22, v172
	s_nop 1
	v_cndmask_b32_e32 v210, v172, v210, vcc
	v_rsq_f32_e32 v210, v210
	s_nop 0
	v_mul_f32_e32 v211, 0x45800000, v210
	v_cndmask_b32_e32 v226, v210, v211, vcc
	v_mul_f32_e32 v210, 0x4b800000, v173
	v_cmp_gt_f32_e32 vcc, s22, v173
	s_nop 1
	v_cndmask_b32_e32 v210, v173, v210, vcc
	v_rsq_f32_e32 v210, v210
	s_nop 0
	v_mul_f32_e32 v211, 0x45800000, v210
	v_cndmask_b32_e32 v228, v210, v211, vcc
	v_lshlrev_b32_e32 v212, 16, v156
	v_and_b32_e32 v213, 0xffff0000, v156
	v_lshlrev_b32_e32 v214, 16, v157
	v_and_b32_e32 v215, 0xffff0000, v157
	v_pk_mul_f32 v[212:213], v[226:227], v[212:213] op_sel_hi:[0,1]
	v_pk_mul_f32 v[214:215], v[226:227], v[214:215] op_sel_hi:[0,1]
	v_pk_mul_f32 v[212:213], v[212:213], v[12:13]
	v_pk_mul_f32 v[214:215], v[214:215], v[14:15]
	v_pk_fma_f32 v[124:125], v[188:189], v[212:213], v[124:125]
	v_pk_fma_f32 v[126:127], v[190:191], v[214:215], v[126:127]
	global_store_dwordx4 v2, v[124:127], s[16:17] offset:-4096
	v_lshlrev_b32_e32 v216, 16, v158
	v_and_b32_e32 v217, 0xffff0000, v158
	v_lshlrev_b32_e32 v218, 16, v159
	v_and_b32_e32 v219, 0xffff0000, v159
	v_pk_mul_f32 v[216:217], v[226:227], v[216:217] op_sel_hi:[0,1]
	v_pk_mul_f32 v[218:219], v[226:227], v[218:219] op_sel_hi:[0,1]
	v_pk_mul_f32 v[216:217], v[216:217], v[16:17]
	v_pk_mul_f32 v[218:219], v[218:219], v[18:19]
	v_pk_fma_f32 v[128:129], v[192:193], v[216:217], v[128:129]
	v_pk_fma_f32 v[130:131], v[194:195], v[218:219], v[130:131]
	global_store_dwordx4 v2, v[128:131], s[16:17] offset:-3072
	v_lshlrev_b32_e32 v212, 16, v160
	v_and_b32_e32 v213, 0xffff0000, v160
	v_lshlrev_b32_e32 v214, 16, v161
	v_and_b32_e32 v215, 0xffff0000, v161
	v_pk_mul_f32 v[212:213], v[226:227], v[212:213] op_sel_hi:[0,1]
	v_pk_mul_f32 v[214:215], v[226:227], v[214:215] op_sel_hi:[0,1]
	v_pk_mul_f32 v[212:213], v[212:213], v[20:21]
	v_pk_mul_f32 v[214:215], v[214:215], v[22:23]
	v_pk_fma_f32 v[132:133], v[196:197], v[212:213], v[132:133]
	v_pk_fma_f32 v[134:135], v[198:199], v[214:215], v[134:135]
	global_store_dwordx4 v2, v[132:135], s[16:17] offset:-2048
	v_lshlrev_b32_e32 v216, 16, v162
	v_and_b32_e32 v217, 0xffff0000, v162
	v_lshlrev_b32_e32 v218, 16, v163
	v_and_b32_e32 v219, 0xffff0000, v163
	v_pk_mul_f32 v[216:217], v[226:227], v[216:217] op_sel_hi:[0,1]
	v_pk_mul_f32 v[218:219], v[226:227], v[218:219] op_sel_hi:[0,1]
	v_pk_mul_f32 v[216:217], v[216:217], v[24:25]
	v_pk_mul_f32 v[218:219], v[218:219], v[26:27]
	v_pk_fma_f32 v[136:137], v[200:201], v[216:217], v[136:137]
	v_pk_fma_f32 v[138:139], v[202:203], v[218:219], v[138:139]
	global_store_dwordx4 v2, v[136:139], s[16:17] offset:-1024
	v_lshlrev_b32_e32 v212, 16, v164
	v_and_b32_e32 v213, 0xffff0000, v164
	v_lshlrev_b32_e32 v214, 16, v165
	v_and_b32_e32 v215, 0xffff0000, v165
	v_pk_mul_f32 v[212:213], v[228:229], v[212:213] op_sel_hi:[0,1]
	v_pk_mul_f32 v[214:215], v[228:229], v[214:215] op_sel_hi:[0,1]
	v_pk_mul_f32 v[212:213], v[212:213], v[12:13]
	v_pk_mul_f32 v[214:215], v[214:215], v[14:15]
	v_pk_fma_f32 v[140:141], v[188:189], v[212:213], v[140:141]
	v_pk_fma_f32 v[142:143], v[190:191], v[214:215], v[142:143]
	global_store_dwordx4 v2, v[140:143], s[16:17] offset:0
	v_lshlrev_b32_e32 v216, 16, v166
	v_and_b32_e32 v217, 0xffff0000, v166
	v_lshlrev_b32_e32 v218, 16, v167
	v_and_b32_e32 v219, 0xffff0000, v167
	v_pk_mul_f32 v[216:217], v[228:229], v[216:217] op_sel_hi:[0,1]
	v_pk_mul_f32 v[218:219], v[228:229], v[218:219] op_sel_hi:[0,1]
	v_pk_mul_f32 v[216:217], v[216:217], v[16:17]
	v_pk_mul_f32 v[218:219], v[218:219], v[18:19]
	v_pk_fma_f32 v[144:145], v[192:193], v[216:217], v[144:145]
	v_pk_fma_f32 v[146:147], v[194:195], v[218:219], v[146:147]
	global_store_dwordx4 v2, v[144:147], s[16:17] offset:1024
	v_lshlrev_b32_e32 v212, 16, v168
	v_and_b32_e32 v213, 0xffff0000, v168
	v_lshlrev_b32_e32 v214, 16, v169
	v_and_b32_e32 v215, 0xffff0000, v169
	v_pk_mul_f32 v[212:213], v[228:229], v[212:213] op_sel_hi:[0,1]
	v_pk_mul_f32 v[214:215], v[228:229], v[214:215] op_sel_hi:[0,1]
	v_pk_mul_f32 v[212:213], v[212:213], v[20:21]
	v_pk_mul_f32 v[214:215], v[214:215], v[22:23]
	v_pk_fma_f32 v[148:149], v[196:197], v[212:213], v[148:149]
	v_pk_fma_f32 v[150:151], v[198:199], v[214:215], v[150:151]
	global_store_dwordx4 v2, v[148:151], s[16:17] offset:2048
	v_lshlrev_b32_e32 v216, 16, v170
	v_and_b32_e32 v217, 0xffff0000, v170
	v_lshlrev_b32_e32 v218, 16, v171
	v_and_b32_e32 v219, 0xffff0000, v171
	v_pk_mul_f32 v[216:217], v[228:229], v[216:217] op_sel_hi:[0,1]
	v_pk_mul_f32 v[218:219], v[228:229], v[218:219] op_sel_hi:[0,1]
	v_pk_mul_f32 v[216:217], v[216:217], v[24:25]
	v_pk_mul_f32 v[218:219], v[218:219], v[26:27]
	v_pk_fma_f32 v[152:153], v[200:201], v[216:217], v[152:153]
	v_pk_fma_f32 v[154:155], v[202:203], v[218:219], v[154:155]
	global_store_dwordx4 v2, v[152:155], s[16:17] offset:3072
